# v28 + first V-fragment LDS reads of each PV stage issued right after the last QK MFMA (latency covered by row-sum/pack VALU)
# speedup vs baseline: 1.0131x; 1.0007x over previous
; __device__ __forceinline__ void finishSM(f32x16& p0, f32x16& p1, float alpha, float& l_reg, bf16x8& pa0, bf16x8& pa1, bf16x8& pa2, bf16x8& pa3) {
; #pragma unroll
;     for (int r = 0; r < 16; ++r) p1[r] = __builtin_amdgcn_exp2f(p1[r]);
;     float ps = 0;
; #pragma unroll
;     for (int r = 0; r < 16; ++r) ps += p0[r];
; #pragma unroll
;     for (int r = 0; r < 16; ++r) ps += p1[r];
;     { auto rr = __builtin_amdgcn_permlane32_swap(__float_as_uint(ps), __float_as_uint(ps), false, false);
;       ps = __uint_as_float(rr[0]) + __uint_as_float(rr[1]); }
;     l_reg = l_reg * alpha + ps;
;     ...
;     PK4(p0, 0, pa0); PK4(p0, 8, pa1); PK4(p1, 0, pa2); PK4(p1, 8, pa3);
;     ...
; }
; template <int KB, bool SK, bool ROPE, bool QHALF>
; __device__ __forceinline__ void qkt(f32x16& p0, f32x16& p1, const char* lds, int r32, int hi, const bf16x8* qr, const char* qrl, bool act) {
;     ...
;     const char* kb[4];
; #pragma unroll
;     for (int dd = 0; dd < 4; ++dd) kb[dd] = lds + OFF_K + KB * SHM_K + KSWZ(r32, (dd * 16 + hi * 8) * 2);
; #pragma unroll
;     for (int d0 = 0; d0 < 8; ++d0) { const char* a = kb[d0 & 3] + (d0 >> 2) * 128;
;         bf16x8 b0 = *reinterpret_cast<const bf16x8*>(a);
;         bf16x8 b1 = *reinterpret_cast<const bf16x8*>(a + 32 * 256);
;         bf16x8 qf;
;         if constexpr (QHALF) { if (d0 >= 4) qf = *reinterpret_cast<const bf16x8*>(qrl + (d0 - 4) * 1024); else qf = qr[d0]; } else qf = qr[d0];
;         p0 = __builtin_amdgcn_mfma_f32_32x32x16_bf16(b0, qf, p0, 0, 0, 0);
;         p1 = __builtin_amdgcn_mfma_f32_32x32x16_bf16(b1, qf, p1, 0, 0, 0); }
;     if constexpr (ROPE) {
; #pragma unroll
;         for (int d0 = 0; d0 < 4; ++d0) { const char* a = lds + OFF_KR + KB * SHM_KR + KRSWZ(r32, 2 * d0 + hi);
;             bf16x8 b0 = *reinterpret_cast<const bf16x8*>(a);
;             bf16x8 b1 = *reinterpret_cast<const bf16x8*>(a + 32 * 128);
;             const bf16x8 qf = *reinterpret_cast<const bf16x8*>(qrl + d0 * 1024);
;             p0 = __builtin_amdgcn_mfma_f32_32x32x16_bf16(b0, qf, p0, 0, 0, 0);
;             p1 = __builtin_amdgcn_mfma_f32_32x32x16_bf16(b1, qf, p1, 0, 0, 0); }
.Lmy_nobar_0:
.LBB0_525:
	ds_read_b128 v[4:7], v213 offset:49152
	ds_read_b128 v[8:11], v213 offset:57344
	s_add_i32 s10, 0, 0x12800
	v_exp_f32_e32 v122, v132
	v_exp_f32_e32 v123, v133
	s_waitcnt lgkmcnt(1)
	v_mfma_f32_32x32x16_bf16 v[102:117], v[4:7], v[174:177], 0
	v_exp_f32_e32 v124, v130
	v_exp_f32_e32 v125, v131
	v_exp_f32_e32 v126, v126
	v_exp_f32_e32 v127, v127
	v_exp_f32_e32 v128, v128
	v_exp_f32_e32 v129, v129
	s_add_i32 s6, s48, 0xffffff60
	s_waitcnt lgkmcnt(0)
	v_mfma_f32_32x32x16_bf16 v[86:101], v[8:11], v[174:177], 0
	ds_read_b128 v[4:7], v214 offset:49152
	ds_read_b128 v[8:11], v214 offset:57344
	s_add_i32 s7, s48, 0xffffff9f
	s_waitcnt lgkmcnt(1)
	v_mfma_f32_32x32x16_bf16 v[102:117], v[4:7], v[170:173], v[102:117]
	s_waitcnt lgkmcnt(0)
	v_mfma_f32_32x32x16_bf16 v[86:101], v[8:11], v[170:173], v[86:101]
	ds_read_b128 v[4:7], v215 offset:49152
	ds_read_b128 v[8:11], v215 offset:57344
	s_waitcnt lgkmcnt(1)
	v_mfma_f32_32x32x16_bf16 v[102:117], v[4:7], v[166:169], v[102:117]
	s_waitcnt lgkmcnt(0)
	v_mfma_f32_32x32x16_bf16 v[86:101], v[8:11], v[166:169], v[86:101]
	ds_read_b128 v[4:7], v216 offset:49152
	ds_read_b128 v[8:11], v216 offset:57344
	s_waitcnt lgkmcnt(1)
	v_mfma_f32_32x32x16_bf16 v[102:117], v[4:7], v[162:165], v[102:117]
	s_waitcnt lgkmcnt(0)
	v_mfma_f32_32x32x16_bf16 v[86:101], v[8:11], v[162:165], v[86:101]
	ds_read_b128 v[4:7], v213 offset:49280
	ds_read_b128 v[8:11], v213 offset:57472
	s_waitcnt lgkmcnt(1)
	v_mfma_f32_32x32x16_bf16 v[102:117], v[4:7], v[158:161], v[102:117]
	s_waitcnt lgkmcnt(0)
	v_mfma_f32_32x32x16_bf16 v[86:101], v[8:11], v[158:161], v[86:101]
	ds_read_b128 v[4:7], v214 offset:49280
	ds_read_b128 v[8:11], v214 offset:57472
	s_waitcnt lgkmcnt(1)
	v_mfma_f32_32x32x16_bf16 v[102:117], v[4:7], v[154:157], v[102:117]
	s_waitcnt lgkmcnt(0)
	v_mfma_f32_32x32x16_bf16 v[86:101], v[8:11], v[154:157], v[86:101]
	ds_read_b128 v[4:7], v215 offset:49280
	ds_read_b128 v[8:11], v215 offset:57472
	s_waitcnt lgkmcnt(1)
	v_mfma_f32_32x32x16_bf16 v[102:117], v[4:7], v[150:153], v[102:117]
	s_waitcnt lgkmcnt(0)
	v_mfma_f32_32x32x16_bf16 v[86:101], v[8:11], v[150:153], v[86:101]
	ds_read_b128 v[4:7], v216 offset:49280
	ds_read_b128 v[8:11], v216 offset:57472
	s_waitcnt lgkmcnt(1)
	v_mfma_f32_32x32x16_bf16 v[102:117], v[4:7], v[146:149], v[102:117]
	s_waitcnt lgkmcnt(0)
	v_mfma_f32_32x32x16_bf16 v[86:101], v[8:11], v[146:149], v[86:101]
	v_add_u32_e32 v8, s10, v217
	ds_read_b128 v[4:7], v8
	ds_read_b128 v[8:11], v8 offset:4096
	ds_read_b128 v[12:15], v202
	s_waitcnt lgkmcnt(0)
	v_mfma_f32_32x32x16_bf16 v[102:117], v[4:7], v[12:15], v[102:117]
	v_mfma_f32_32x32x16_bf16 v[86:101], v[8:11], v[12:15], v[86:101]
	v_add_u32_e32 v8, s10, v218
	ds_read_b128 v[4:7], v8
	ds_read_b128 v[8:11], v8 offset:4096
	ds_read_b128 v[12:15], v202 offset:1024
	s_waitcnt lgkmcnt(0)
	v_mfma_f32_32x32x16_bf16 v[102:117], v[4:7], v[12:15], v[102:117]
	v_mfma_f32_32x32x16_bf16 v[86:101], v[8:11], v[12:15], v[86:101]
	v_add_u32_e32 v8, s10, v219
	ds_read_b128 v[4:7], v8
	ds_read_b128 v[8:11], v8 offset:4096
	ds_read_b128 v[12:15], v202 offset:2048
	s_waitcnt lgkmcnt(0)
	v_mfma_f32_32x32x16_bf16 v[102:117], v[4:7], v[12:15], v[102:117]
	v_mfma_f32_32x32x16_bf16 v[86:101], v[8:11], v[12:15], v[86:101]
	v_add_u32_e32 v8, s10, v220
	ds_read_b128 v[4:7], v8
	ds_read_b128 v[8:11], v8 offset:4096
	ds_read_b128 v[12:15], v202 offset:3072
	s_waitcnt lgkmcnt(0)
	v_mfma_f32_32x32x16_bf16 v[102:117], v[4:7], v[12:15], v[102:117]
	v_exp_f32_e32 v4, v140
	v_exp_f32_e32 v5, v141
	v_exp_f32_e32 v6, v138
	v_exp_f32_e32 v7, v139
	v_mfma_f32_32x32x16_bf16 v[86:101], v[8:11], v[12:15], v[86:101]
	ds_read_b64_tr_b16 v[232:233], v210 offset:0
	ds_read_b64_tr_b16 v[234:235], v210 offset:0x800
	ds_read_b64_tr_b16 v[236:237], v210 offset:0x1000
	ds_read_b64_tr_b16 v[238:239], v210 offset:0x1800
	ds_read_b64_tr_b16 v[240:241], v210 offset:0x2000
	ds_read_b64_tr_b16 v[242:243], v210 offset:0x2800
	ds_read_b64_tr_b16 v[244:245], v210 offset:0x3000
	ds_read_b64_tr_b16 v[246:247], v210 offset:0x3800
	v_add_f32_e32 v12, 0, v188
	v_add_f32_e32 v12, v228, v12
	v_add_f32_e32 v12, v186, v12
	v_add_f32_e32 v12, v189, v12
	v_add_f32_e32 v12, v185, v12
	v_add_f32_e32 v12, v187, v12
	v_add_f32_e32 v12, v183, v12
	v_add_f32_e32 v12, v184, v12
	v_add_f32_e32 v12, v179, v12
	v_add_f32_e32 v12, v182, v12
	v_add_f32_e32 v12, v144, v12
	v_add_f32_e32 v12, v180, v12
	v_add_f32_e32 v12, v142, v12
	v_add_f32_e32 v12, v181, v12
	v_add_f32_e32 v12, v143, v12
	v_add_f32_e32 v12, v145, v12
	v_exp_f32_e32 v8, v136
	v_add_f32_e32 v12, v4, v12
	v_exp_f32_e32 v9, v137
	v_add_f32_e32 v12, v5, v12
	v_exp_f32_e32 v10, v134
	v_add_f32_e32 v12, v6, v12
	v_exp_f32_e32 v11, v135
	v_add_f32_e32 v12, v7, v12
	v_add_f32_e32 v12, v8, v12
	v_add_f32_e32 v12, v9, v12
	v_add_f32_e32 v12, v10, v12
	v_add_f32_e32 v12, v11, v12
	v_add_f32_e32 v12, v122, v12
	v_add_f32_e32 v12, v123, v12
	v_add_f32_e32 v12, v124, v12
	v_add_f32_e32 v12, v125, v12
	v_add_f32_e32 v12, v126, v12
	v_add_f32_e32 v12, v127, v12
	v_add_f32_e32 v12, v128, v12
	v_add_f32_e32 v195, v129, v12
	v_mov_b32_e32 v226, v195
	s_nop 1
	v_permlane32_swap_b32_e32 v195, v226
	v_cvt_pk_bf16_f32 v12, v188, v228
	v_cvt_pk_bf16_f32 v13, v186, v189
	v_cvt_pk_bf16_f32 v14, v185, v187
	v_cvt_pk_bf16_f32 v15, v183, v184
	v_cvt_pk_bf16_f32 v82, v179, v182
	v_cvt_pk_bf16_f32 v83, v144, v180
	v_cvt_pk_bf16_f32 v84, v142, v181
	v_cvt_pk_bf16_f32 v85, v143, v145
	v_cvt_pk_bf16_f32 v118, v4, v5
	v_cvt_pk_bf16_f32 v119, v6, v7
	v_cvt_pk_bf16_f32 v120, v8, v9
	v_cvt_pk_bf16_f32 v121, v10, v11
	v_cvt_pk_bf16_f32 v122, v122, v123
	v_cvt_pk_bf16_f32 v123, v124, v125
	v_cvt_pk_bf16_f32 v124, v126, v127
	v_cvt_pk_bf16_f32 v125, v128, v129
	s_nop 0
	v_permlane32_swap_b32_e32 v12, v14
	v_permlane32_swap_b32_e32 v13, v15
	v_permlane32_swap_b32_e32 v82, v84
	v_permlane32_swap_b32_e32 v83, v85
	v_permlane32_swap_b32_e32 v118, v120
	v_permlane32_swap_b32_e32 v119, v121
	v_permlane32_swap_b32_e32 v122, v124
	v_permlane32_swap_b32_e32 v123, v125
	s_add_i32 s10, s48, 0xffffffa0
	s_sub_i32 s72, s48, 64
	s_mov_b32 s73, s11
	s_lshl_b64 s[50:51], s[10:11], 12
	s_lshl_b64 s[72:73], s[72:73], 12
	v_lshl_add_u64 v[4:5], v[196:197], 0, s[50:51]
	v_lshl_add_u64 v[8:9], v[196:197], 0, s[72:73]
	v_lshl_add_u64 v[126:127], v[198:199], 0, s[50:51]
	s_add_i32 m0, s37, 0x8000
	global_load_dwordx4 v[4:7], v[4:5], off
	s_nop 0
	global_load_dwordx4 v[8:11], v[8:9], off
	s_lshl_b64 s[50:51], s[10:11], 7
	global_load_lds_dwordx4 v[126:127], off
	v_lshl_add_u64 v[126:127], v[198:199], 0, s[72:73]
	s_add_i32 m0, s37, 0xa000
	s_nop 0
	global_load_lds_dwordx4 v[126:127], off
	v_lshl_add_u64 v[126:127], v[16:17], 0, s[50:51]
	s_add_i32 m0, s37, 0x10800
	s_nop 0
	global_load_lds_dwordx4 v[126:127], off
	s_waitcnt lgkmcnt(0)
; __device__ __forceinline__ void mask_tile(f32x16& p0, f32x16& p1, int dq, unsigned W) {
;     const float NEG = -__builtin_inff();
; #pragma unroll
;     for (int r = 0; r < 16; ++r) {
;         const int c = (r & 3) + 8 * (r >> 2);
;         if ((unsigned)(dq - c) >= W) p0[r] = NEG;
;         if ((unsigned)(dq - c - 32) >= W) p1[r] = NEG;
;     }
; }
; template <int VB, bool SK>
; __device__ __forceinline__ void pv_tile(f32x16* o, int vb0, bf16x8 pa0, bf16x8 pa1, bf16x8 pa2, bf16x8 pa3, bool act) {
;     if (SK && !act) return;
;     ...
;     if (ATT_PRIO) __builtin_amdgcn_s_setprio(1);
;     PV_D0(0); PV_D0(1); PV_D0(2); PV_D0(3);
	s_nop 0
	v_mfma_f32_32x32x16_bf16 v[66:81], v[12:15], v[232:235], v[66:81]
	ds_read_b64_tr_b16 v[126:127], v210 offset:0x200
	ds_read_b64_tr_b16 v[128:129], v210 offset:0xa00
	v_mfma_f32_32x32x16_bf16 v[66:81], v[82:85], v[236:239], v[66:81]
	ds_read_b64_tr_b16 v[130:131], v210 offset:0x1200
	ds_read_b64_tr_b16 v[132:133], v210 offset:0x1a00
	v_mfma_f32_32x32x16_bf16 v[66:81], v[118:121], v[240:243], v[66:81]
	ds_read_b64_tr_b16 v[134:135], v210 offset:0x2200
	ds_read_b64_tr_b16 v[136:137], v210 offset:0x2a00
	ds_read_b64_tr_b16 v[142:143], v210 offset:0x3200
	ds_read_b64_tr_b16 v[144:145], v210 offset:0x3a00
	s_waitcnt lgkmcnt(0)
	v_mfma_f32_32x32x16_bf16 v[66:81], v[122:125], v[244:247], v[66:81]
	v_mfma_f32_32x32x16_bf16 v[50:65], v[12:15], v[126:129], v[50:65]
	ds_read_b64_tr_b16 v[126:127], v210 offset:0x400
	ds_read_b64_tr_b16 v[128:129], v210 offset:0xc00
	v_mfma_f32_32x32x16_bf16 v[50:65], v[82:85], v[130:133], v[50:65]
	ds_read_b64_tr_b16 v[130:131], v210 offset:0x1400
	ds_read_b64_tr_b16 v[132:133], v210 offset:0x1c00
	v_mfma_f32_32x32x16_bf16 v[50:65], v[118:121], v[134:137], v[50:65]
	ds_read_b64_tr_b16 v[134:135], v210 offset:0x2400
	ds_read_b64_tr_b16 v[136:137], v210 offset:0x2c00
	ds_read_b64_tr_b16 v[138:139], v210 offset:0x3400
	ds_read_b64_tr_b16 v[140:141], v210 offset:0x3c00
	s_waitcnt lgkmcnt(0)
	v_mfma_f32_32x32x16_bf16 v[50:65], v[122:125], v[142:145], v[50:65]
	v_mfma_f32_32x32x16_bf16 v[34:49], v[12:15], v[126:129], v[34:49]
	ds_read_b64_tr_b16 v[126:127], v210 offset:0x600
	ds_read_b64_tr_b16 v[128:129], v210 offset:0xe00
	v_mfma_f32_32x32x16_bf16 v[34:49], v[82:85], v[130:133], v[34:49]
	ds_read_b64_tr_b16 v[130:131], v210 offset:0x1600
	ds_read_b64_tr_b16 v[132:133], v210 offset:0x1e00
	v_mfma_f32_32x32x16_bf16 v[34:49], v[118:121], v[134:137], v[34:49]
	ds_read_b64_tr_b16 v[134:135], v210 offset:0x2600
	ds_read_b64_tr_b16 v[136:137], v210 offset:0x2e00
	ds_read_b64_tr_b16 v[142:143], v210 offset:0x3600
	ds_read_b64_tr_b16 v[144:145], v210 offset:0x3e00
	s_waitcnt lgkmcnt(0)
	v_mfma_f32_32x32x16_bf16 v[34:49], v[122:125], v[138:141], v[34:49]
	v_mfma_f32_32x32x16_bf16 v[18:33], v[12:15], v[126:129], v[18:33]
	s_cmp_le_i32 s7, s46
	s_cselect_b64 s[50:51], -1, 0
	s_cmp_gt_i32 s6, s18
	s_cselect_b64 s[6:7], -1, 0
	s_and_b64 s[6:7], s[6:7], s[50:51]
	s_and_b64 vcc, exec, s[6:7]
	v_mfma_f32_32x32x16_bf16 v[18:33], v[82:85], v[130:133], v[18:33]
	v_mfma_f32_32x32x16_bf16 v[18:33], v[118:121], v[134:137], v[18:33]
	v_mfma_f32_32x32x16_bf16 v[18:33], v[122:125], v[142:145], v[18:33]
	s_cbranch_vccnz .LBB0_527
	v_add_u32_e32 v12, 0x7b, v193
	v_cmp_gt_u32_e32 vcc, 2.0, v12
	v_add_u32_e32 v12, 0x5b, v193
	s_nop 0
	v_cndmask_b32_e32 v102, v200, v102, vcc
	v_cmp_gt_u32_e32 vcc, 2.0, v12
	v_add_u32_e32 v12, 0x7a, v193
	s_nop 0
	v_cndmask_b32_e32 v86, v200, v86, vcc
	v_cmp_gt_u32_e32 vcc, 2.0, v12
	v_add_u32_e32 v12, 0x5a, v193
	s_nop 0
	v_cndmask_b32_e32 v103, v200, v103, vcc
	v_cmp_gt_u32_e32 vcc, 2.0, v12
	v_add_u32_e32 v12, 0x79, v193
	s_nop 0
	v_cndmask_b32_e32 v87, v200, v87, vcc
	v_cmp_gt_u32_e32 vcc, 2.0, v12
	v_add_u32_e32 v12, 0x59, v193
	s_nop 0
	v_cndmask_b32_e32 v104, v200, v104, vcc
	v_cmp_gt_u32_e32 vcc, 2.0, v12
	v_add_u32_e32 v12, 0x78, v193
	s_nop 0
	v_cndmask_b32_e32 v88, v200, v88, vcc
	v_cmp_gt_u32_e32 vcc, 2.0, v12
	v_add_u32_e32 v12, 0x58, v193
	s_nop 0
	v_cndmask_b32_e32 v105, v200, v105, vcc
	v_cmp_gt_u32_e32 vcc, 2.0, v12
	v_add_u32_e32 v12, 0x73, v193
	s_nop 0
	v_cndmask_b32_e32 v89, v200, v89, vcc
	v_cmp_gt_u32_e32 vcc, 2.0, v12
	v_add_u32_e32 v12, 0x53, v193
	s_nop 0
	v_cndmask_b32_e32 v106, v200, v106, vcc
	v_cmp_gt_u32_e32 vcc, 2.0, v12
	v_add_u32_e32 v12, 0x72, v193
	s_nop 0
	v_cndmask_b32_e32 v90, v200, v90, vcc
	v_cmp_gt_u32_e32 vcc, 2.0, v12
	v_add_u32_e32 v12, 0x52, v193
	s_nop 0
	v_cndmask_b32_e32 v107, v200, v107, vcc
	v_cmp_gt_u32_e32 vcc, 2.0, v12
	v_add_u32_e32 v12, 0x71, v193
	s_nop 0
	v_cndmask_b32_e32 v91, v200, v91, vcc
	v_cmp_gt_u32_e32 vcc, 2.0, v12
	v_add_u32_e32 v12, 0x51, v193
	s_nop 0
	v_cndmask_b32_e32 v108, v200, v108, vcc
	v_cmp_gt_u32_e32 vcc, 2.0, v12
	v_add_u32_e32 v12, 0x70, v193
	s_nop 0
	v_cndmask_b32_e32 v92, v200, v92, vcc
	v_cmp_gt_u32_e32 vcc, 2.0, v12
	v_add_u32_e32 v12, 0x50, v193
	s_nop 0
	v_cndmask_b32_e32 v109, v200, v109, vcc
	v_cmp_gt_u32_e32 vcc, 2.0, v12
	v_add_u32_e32 v12, 0x6b, v193
	s_nop 0
	v_cndmask_b32_e32 v93, v200, v93, vcc
	v_cmp_gt_u32_e32 vcc, 2.0, v12
	v_add_u32_e32 v12, 0x4b, v193
	s_nop 0
	v_cndmask_b32_e32 v110, v200, v110, vcc
	v_cmp_gt_u32_e32 vcc, 2.0, v12
	v_add_u32_e32 v12, 0x6a, v193
	s_nop 0
	v_cndmask_b32_e32 v94, v200, v94, vcc
	v_cmp_gt_u32_e32 vcc, 2.0, v12
	v_add_u32_e32 v12, 0x4a, v193
	s_nop 0
	v_cndmask_b32_e32 v111, v200, v111, vcc
	v_cmp_gt_u32_e32 vcc, 2.0, v12
	v_add_u32_e32 v12, 0x69, v193
	s_nop 0
	v_cndmask_b32_e32 v95, v200, v95, vcc
	v_cmp_gt_u32_e32 vcc, 2.0, v12
	v_add_u32_e32 v12, 0x49, v193
	s_nop 0
	v_cndmask_b32_e32 v112, v200, v112, vcc
	v_cmp_gt_u32_e32 vcc, 2.0, v12
	v_add_u32_e32 v12, 0x68, v193
	s_nop 0
	v_cndmask_b32_e32 v96, v200, v96, vcc
	v_cmp_gt_u32_e32 vcc, 2.0, v12
	v_add_u32_e32 v12, 0x48, v193
	s_nop 0
	v_cndmask_b32_e32 v113, v200, v113, vcc
	v_cmp_gt_u32_e32 vcc, 2.0, v12
	v_add_u32_e32 v12, 0x63, v193
	s_nop 0
	v_cndmask_b32_e32 v97, v200, v97, vcc
	v_cmp_gt_u32_e32 vcc, 2.0, v12
	v_add_u32_e32 v12, 0x43, v193
	s_nop 0
	v_cndmask_b32_e32 v114, v200, v114, vcc
	v_cmp_gt_u32_e32 vcc, 2.0, v12
	v_add_u32_e32 v12, 0x62, v193
	s_nop 0
	v_cndmask_b32_e32 v98, v200, v98, vcc
	v_cmp_gt_u32_e32 vcc, 2.0, v12
	v_add_u32_e32 v12, 0x42, v193
	s_nop 0
	v_cndmask_b32_e32 v115, v200, v115, vcc
	v_cmp_gt_u32_e32 vcc, 2.0, v12
	v_add_u32_e32 v12, 0x61, v193
	s_nop 0
	v_cndmask_b32_e32 v99, v200, v99, vcc
	v_cmp_gt_u32_e32 vcc, 2.0, v12
	v_add_u32_e32 v12, 0x41, v193
	s_nop 0
	v_cndmask_b32_e32 v116, v200, v116, vcc
	v_cmp_gt_u32_e32 vcc, 2.0, v12
	v_add_u32_e32 v12, 0x60, v193
	s_nop 0
	v_cndmask_b32_e32 v100, v200, v100, vcc
	v_cmp_gt_u32_e32 vcc, 2.0, v12
	v_add_u32_e32 v12, 64, v193
	s_nop 0
	v_cndmask_b32_e32 v117, v200, v117, vcc
	v_cmp_gt_u32_e32 vcc, 2.0, v12
	s_nop 1
	v_cndmask_b32_e32 v101, v200, v101, vcc

; template <int MODE>
; __device__ __forceinline__ void partialSM(f32x16& p0, f32x16& p1, float& m_reg, float& mn, float& alpha) {
;     ...
;     constexpr float C2 = 1.4426950408889634f * SCALE;
;     if (__builtin_expect(__all((pmax - m_reg) * SCALE <= THR), 1)) { mn = m_reg; alpha = 1.f; }
;     else { mn = fmaxf(m_reg, pmax); alpha = __builtin_amdgcn_exp2f((m_reg - mn) * C2); m_reg = mn; }
;     const float mnL = -mn * C2;
; #pragma unroll
;     for (int r = 0; r < 16; ++r) p0[r] = fmaf(p0[r], C2, mnL);
; #pragma unroll
;     for (int r = 0; r < 16; ++r) p1[r] = fmaf(p1[r], C2, mnL);
; #pragma unroll
;     for (int r = 0; r < 16; ++r) p0[r] = __builtin_amdgcn_exp2f(p0[r]);
; template <int KB, bool SK, bool ROPE, bool QHALF>
; __device__ __forceinline__ void qkt(f32x16& p0, f32x16& p1, const char* lds, int r32, int hi, const bf16x8* qr, const char* qrl, bool act) {
;     ...
;     const char* kb[4];
; #pragma unroll
;     for (int dd = 0; dd < 4; ++dd) kb[dd] = lds + OFF_K + KB * SHM_K + KSWZ(r32, (dd * 16 + hi * 8) * 2);
; #pragma unroll
;     for (int d0 = 0; d0 < 8; ++d0) { const char* a = kb[d0 & 3] + (d0 >> 2) * 128;
;         bf16x8 b0 = *reinterpret_cast<const bf16x8*>(a);
;         bf16x8 b1 = *reinterpret_cast<const bf16x8*>(a + 32 * 256);
;         bf16x8 qf;
;         if constexpr (QHALF) { if (d0 >= 4) qf = *reinterpret_cast<const bf16x8*>(qrl + (d0 - 4) * 1024); else qf = qr[d0]; } else qf = qr[d0];
;         p0 = __builtin_amdgcn_mfma_f32_32x32x16_bf16(b0, qf, p0, 0, 0, 0);
;         p1 = __builtin_amdgcn_mfma_f32_32x32x16_bf16(b1, qf, p1, 0, 0, 0); }
.LBB0_531:
	v_cndmask_b32_e64 v228, v12, v178, s[6:7]
	v_mul_f32_e32 v12, 0xbdd53b94, v228
	v_fmamk_f32 v82, v102, 0x3dd53b94, v12
	v_fmamk_f32 v83, v103, 0x3dd53b94, v12
	v_fmamk_f32 v84, v104, 0x3dd53b94, v12
	v_fmamk_f32 v85, v105, 0x3dd53b94, v12
	v_fmamk_f32 v118, v106, 0x3dd53b94, v12
	v_fmamk_f32 v119, v107, 0x3dd53b94, v12
	v_fmamk_f32 v120, v108, 0x3dd53b94, v12
	v_fmamk_f32 v121, v109, 0x3dd53b94, v12
	v_fmamk_f32 v122, v110, 0x3dd53b94, v12
	v_fmamk_f32 v123, v111, 0x3dd53b94, v12
	v_fmamk_f32 v112, v112, 0x3dd53b94, v12
	v_fmamk_f32 v113, v113, 0x3dd53b94, v12
	v_fmamk_f32 v114, v114, 0x3dd53b94, v12
	v_fmamk_f32 v115, v115, 0x3dd53b94, v12
	v_fmamk_f32 v116, v116, 0x3dd53b94, v12
	v_fmamk_f32 v117, v117, 0x3dd53b94, v12
	v_fmamk_f32 v102, v86, 0x3dd53b94, v12
	v_fmamk_f32 v103, v87, 0x3dd53b94, v12
	v_fmamk_f32 v104, v88, 0x3dd53b94, v12
	v_fmamk_f32 v110, v89, 0x3dd53b94, v12
	v_fmamk_f32 v111, v90, 0x3dd53b94, v12
	v_fmamk_f32 v14, v91, 0x3dd53b94, v12
	v_fmamk_f32 v15, v92, 0x3dd53b94, v12
	v_fmamk_f32 v105, v93, 0x3dd53b94, v12
	v_fmamk_f32 v106, v94, 0x3dd53b94, v12
	v_fmamk_f32 v107, v95, 0x3dd53b94, v12
	v_fmamk_f32 v108, v96, 0x3dd53b94, v12
	v_fmamk_f32 v109, v97, 0x3dd53b94, v12
	v_exp_f32_e32 v82, v82
	v_exp_f32_e32 v83, v83
	v_exp_f32_e32 v84, v84
	v_exp_f32_e32 v85, v85
	v_exp_f32_e32 v86, v118
	v_exp_f32_e32 v87, v119
	v_exp_f32_e32 v88, v120
	v_exp_f32_e32 v89, v121
	v_exp_f32_e32 v90, v122
	v_exp_f32_e32 v91, v123
	v_exp_f32_e32 v92, v112
	v_exp_f32_e32 v93, v113
	v_exp_f32_e32 v94, v114
	v_exp_f32_e32 v95, v115
	v_exp_f32_e32 v96, v116
	v_exp_f32_e32 v97, v117
	v_fmamk_f32 v13, v98, 0x3dd53b94, v12
	v_fmamk_f32 v112, v99, 0x3dd53b94, v12
	v_fmamk_f32 v113, v100, 0x3dd53b94, v12
	v_fmac_f32_e32 v12, 0x3dd53b94, v101
	s_waitcnt lgkmcnt(0)
	ds_read_b128 v[98:101], v213 offset:32768
	ds_read_b128 v[114:117], v213 offset:40960
	v_exp_f32_e32 v105, v105
	v_exp_f32_e32 v106, v106
	v_exp_f32_e32 v107, v107
	s_waitcnt lgkmcnt(1)
	v_mfma_f32_32x32x16_bf16 v[130:145], v[98:101], v[174:177], 0
	ds_read_b128 v[98:101], v214 offset:32768
	ds_read_b128 v[178:181], v214 offset:40960
	v_exp_f32_e32 v108, v108
	v_exp_f32_e32 v109, v109
	s_waitcnt lgkmcnt(2)
	v_mfma_f32_32x32x16_bf16 v[114:129], v[114:117], v[174:177], 0
	s_waitcnt lgkmcnt(1)
	v_mfma_f32_32x32x16_bf16 v[130:145], v[98:101], v[170:173], v[130:145]
	s_waitcnt lgkmcnt(0)
	v_mfma_f32_32x32x16_bf16 v[114:129], v[178:181], v[170:173], v[114:129]
	ds_read_b128 v[98:101], v215 offset:32768
	ds_read_b128 v[178:181], v215 offset:40960
	s_waitcnt lgkmcnt(1)
	v_mfma_f32_32x32x16_bf16 v[130:145], v[98:101], v[166:169], v[130:145]
	s_waitcnt lgkmcnt(0)
	v_mfma_f32_32x32x16_bf16 v[114:129], v[178:181], v[166:169], v[114:129]
	ds_read_b128 v[98:101], v216 offset:32768
	ds_read_b128 v[178:181], v216 offset:40960
	s_waitcnt lgkmcnt(1)
	v_mfma_f32_32x32x16_bf16 v[130:145], v[98:101], v[162:165], v[130:145]
	s_waitcnt lgkmcnt(0)
	v_mfma_f32_32x32x16_bf16 v[114:129], v[178:181], v[162:165], v[114:129]
	ds_read_b128 v[98:101], v213 offset:32896
	ds_read_b128 v[178:181], v213 offset:41088
	s_waitcnt lgkmcnt(1)
	v_mfma_f32_32x32x16_bf16 v[130:145], v[98:101], v[158:161], v[130:145]
	s_waitcnt lgkmcnt(0)
	v_mfma_f32_32x32x16_bf16 v[114:129], v[178:181], v[158:161], v[114:129]
	ds_read_b128 v[98:101], v214 offset:32896
	ds_read_b128 v[178:181], v214 offset:41088
	s_waitcnt lgkmcnt(1)
	v_mfma_f32_32x32x16_bf16 v[130:145], v[98:101], v[154:157], v[130:145]
	s_waitcnt lgkmcnt(0)
	v_mfma_f32_32x32x16_bf16 v[114:129], v[178:181], v[154:157], v[114:129]
	ds_read_b128 v[98:101], v215 offset:32896
	ds_read_b128 v[178:181], v215 offset:41088
	s_waitcnt lgkmcnt(1)
	v_mfma_f32_32x32x16_bf16 v[130:145], v[98:101], v[150:153], v[130:145]
	s_waitcnt lgkmcnt(0)
	v_mfma_f32_32x32x16_bf16 v[114:129], v[178:181], v[150:153], v[114:129]
	ds_read_b128 v[98:101], v216 offset:32896
	ds_read_b128 v[178:181], v216 offset:41088
	s_waitcnt lgkmcnt(1)
	v_mfma_f32_32x32x16_bf16 v[130:145], v[98:101], v[146:149], v[130:145]
	s_waitcnt lgkmcnt(0)
	v_mfma_f32_32x32x16_bf16 v[114:129], v[178:181], v[146:149], v[114:129]
	ds_read_b128 v[98:101], v222
	ds_read_b128 v[178:181], v222 offset:4096
	ds_read_b128 v[182:185], v202
	s_waitcnt lgkmcnt(0)
	v_mfma_f32_32x32x16_bf16 v[130:145], v[98:101], v[182:185], v[130:145]
	v_mfma_f32_32x32x16_bf16 v[114:129], v[178:181], v[182:185], v[114:129]
	ds_read_b128 v[98:101], v223
	ds_read_b128 v[178:181], v223 offset:4096
	ds_read_b128 v[182:185], v202 offset:1024
	s_waitcnt lgkmcnt(0)
	v_mfma_f32_32x32x16_bf16 v[130:145], v[98:101], v[182:185], v[130:145]
	v_mfma_f32_32x32x16_bf16 v[114:129], v[178:181], v[182:185], v[114:129]
	ds_read_b128 v[98:101], v224
	ds_read_b128 v[178:181], v224 offset:4096
	ds_read_b128 v[182:185], v202 offset:2048
	s_waitcnt lgkmcnt(0)
	v_mfma_f32_32x32x16_bf16 v[130:145], v[98:101], v[182:185], v[130:145]
	v_mfma_f32_32x32x16_bf16 v[114:129], v[178:181], v[182:185], v[114:129]
	ds_read_b128 v[98:101], v225
	ds_read_b128 v[178:181], v225 offset:4096
	ds_read_b128 v[182:185], v202 offset:3072
	s_waitcnt lgkmcnt(0)
; __device__ __forceinline__ void finishSM(f32x16& p0, f32x16& p1, float alpha, float& l_reg, bf16x8& pa0, bf16x8& pa1, bf16x8& pa2, bf16x8& pa3) {
; #pragma unroll
;     for (int r = 0; r < 16; ++r) p1[r] = __builtin_amdgcn_exp2f(p1[r]);
;     float ps = 0;
; #pragma unroll
;     for (int r = 0; r < 16; ++r) ps += p0[r];
; #pragma unroll
;     for (int r = 0; r < 16; ++r) ps += p1[r];
;     { auto rr = __builtin_amdgcn_permlane32_swap(__float_as_uint(ps), __float_as_uint(ps), false, false);
;       ps = __uint_as_float(rr[0]) + __uint_as_float(rr[1]); }
;     l_reg = l_reg * alpha + ps;
;     ...
;     PK4(p0, 0, pa0); PK4(p0, 8, pa1); PK4(p1, 0, pa2); PK4(p1, 8, pa3);
;     ...
; }
; template <int VB, bool SK>
; __device__ __forceinline__ void pv_tile(f32x16* o, int vb0, bf16x8 pa0, bf16x8 pa1, bf16x8 pa2, bf16x8 pa3, bool act) {
;     if (SK && !act) return;
	v_mfma_f32_32x32x16_bf16 v[130:145], v[98:101], v[182:185], v[130:145]
	ds_read_b64_tr_b16 v[232:233], v210 offset:0x4000
	ds_read_b64_tr_b16 v[234:235], v210 offset:0x4800
	ds_read_b64_tr_b16 v[236:237], v210 offset:0x5000
	ds_read_b64_tr_b16 v[238:239], v210 offset:0x5800
	ds_read_b64_tr_b16 v[240:241], v210 offset:0x6000
	ds_read_b64_tr_b16 v[242:243], v210 offset:0x6800
	ds_read_b64_tr_b16 v[244:245], v210 offset:0x7000
	ds_read_b64_tr_b16 v[246:247], v210 offset:0x7800
	v_exp_f32_e32 v98, v102
	v_exp_f32_e32 v102, v111
	v_exp_f32_e32 v111, v112
	v_exp_f32_e32 v112, v113
	v_exp_f32_e32 v113, v12
	v_add_f32_e32 v12, 0, v82
	v_add_f32_e32 v12, v83, v12
	v_add_f32_e32 v12, v84, v12
	v_add_f32_e32 v12, v85, v12
	v_add_f32_e32 v12, v86, v12
	v_add_f32_e32 v12, v87, v12
	v_add_f32_e32 v12, v88, v12
	v_add_f32_e32 v12, v89, v12
	v_add_f32_e32 v12, v90, v12
	v_add_f32_e32 v12, v91, v12
	v_add_f32_e32 v12, v92, v12
	v_add_f32_e32 v12, v93, v12
	v_add_f32_e32 v12, v94, v12
	v_exp_f32_e32 v99, v103
	v_add_f32_e32 v12, v95, v12
	v_exp_f32_e32 v100, v104
	v_add_f32_e32 v12, v96, v12
	v_exp_f32_e32 v101, v110
	v_add_f32_e32 v12, v97, v12
	v_add_f32_e32 v12, v98, v12
	v_exp_f32_e32 v103, v14
	v_add_f32_e32 v12, v99, v12
	v_exp_f32_e32 v104, v15
	v_add_f32_e32 v12, v100, v12
	v_add_f32_e32 v12, v101, v12
	v_add_f32_e32 v12, v102, v12
	v_add_f32_e32 v12, v103, v12
	v_add_f32_e32 v12, v104, v12
	v_add_f32_e32 v12, v105, v12
	v_exp_f32_e32 v110, v13
	v_add_f32_e32 v12, v106, v12
	v_add_f32_e32 v12, v107, v12
	v_mfma_f32_32x32x16_bf16 v[114:129], v[178:181], v[182:185], v[114:129]
	v_add_f32_e32 v12, v108, v12
	v_add_f32_e32 v12, v109, v12
	v_add_f32_e32 v12, v110, v12
	v_add_f32_e32 v12, v111, v12
	v_add_f32_e32 v12, v112, v12
	v_add_f32_e32 v229, v113, v12
	v_mov_b32_e32 v230, v229
	v_cvt_pk_bf16_f32 v12, v82, v83
	v_cvt_pk_bf16_f32 v13, v84, v85
	v_cvt_pk_bf16_f32 v14, v86, v87
	v_cvt_pk_bf16_f32 v15, v88, v89
	v_cvt_pk_bf16_f32 v178, v90, v91
	v_cvt_pk_bf16_f32 v179, v92, v93
	v_cvt_pk_bf16_f32 v180, v94, v95
	v_cvt_pk_bf16_f32 v181, v96, v97
	v_cvt_pk_bf16_f32 v182, v98, v99
	v_cvt_pk_bf16_f32 v183, v100, v101
	v_cvt_pk_bf16_f32 v184, v102, v103
	v_cvt_pk_bf16_f32 v185, v104, v105
	v_cvt_pk_bf16_f32 v186, v106, v107
	v_cvt_pk_bf16_f32 v187, v108, v109
	v_cvt_pk_bf16_f32 v188, v110, v111
	v_cvt_pk_bf16_f32 v189, v112, v113
	s_nop 1
	v_permlane32_swap_b32_e32 v229, v230
	v_permlane32_swap_b32_e32 v12, v14
	v_permlane32_swap_b32_e32 v13, v15
	v_permlane32_swap_b32_e32 v178, v180
	v_permlane32_swap_b32_e32 v179, v181
	v_permlane32_swap_b32_e32 v182, v184
	v_permlane32_swap_b32_e32 v183, v185
	v_permlane32_swap_b32_e32 v186, v188
	v_permlane32_swap_b32_e32 v187, v189
	s_add_i32 s6, s36, 1
	s_cmp_lt_i32 s6, s71
	s_cselect_b64 s[50:51], -1, 0
	s_cmp_ge_i32 s6, s71
	s_cbranch_scc1 .LBB0_533
	s_sub_i32 s6, s48, 32
	s_mov_b32 s7, s11
	s_mov_b32 s49, s11
	s_lshl_b64 s[72:73], s[6:7], 12
	s_lshl_b64 s[74:75], s[48:49], 12
	v_lshl_add_u64 v[4:5], v[196:197], 0, s[72:73]
	v_lshl_add_u64 v[8:9], v[196:197], 0, s[74:75]
	v_lshl_add_u64 v[248:249], v[198:199], 0, s[72:73]
	s_add_i32 m0, s37, 0xc000
	global_load_dwordx4 v[4:7], v[4:5], off
	s_nop 0
	global_load_dwordx4 v[8:11], v[8:9], off
	s_lshl_b64 s[6:7], s[6:7], 7
	global_load_lds_dwordx4 v[248:249], off
	v_lshl_add_u64 v[248:249], v[198:199], 0, s[74:75]
	s_add_i32 m0, s37, 0xe000
	s_nop 0
	global_load_lds_dwordx4 v[248:249], off
	v_lshl_add_u64 v[248:249], v[16:17], 0, s[6:7]
	s_add_i32 m0, s37, 0x12800
	s_nop 0
	global_load_lds_dwordx4 v[248:249], off
; __device__ __forceinline__ void mask_tile(f32x16& p0, f32x16& p1, int dq, unsigned W) {
;     const float NEG = -__builtin_inff();
; #pragma unroll
;     for (int r = 0; r < 16; ++r) {
;         const int c = (r & 3) + 8 * (r >> 2);
;         if ((unsigned)(dq - c) >= W) p0[r] = NEG;
;         if ((unsigned)(dq - c - 32) >= W) p1[r] = NEG;
;     }
; }
; template <int VB, bool SK>
; __device__ __forceinline__ void pv_tile(f32x16* o, int vb0, bf16x8 pa0, bf16x8 pa1, bf16x8 pa2, bf16x8 pa3, bool act) {
;     if (SK && !act) return;
;     ...
;     if (ATT_PRIO) __builtin_amdgcn_s_setprio(1);
;     PV_D0(0); PV_D0(1); PV_D0(2); PV_D0(3);
.LBB0_533:
	s_waitcnt lgkmcnt(0)
	s_sub_i32 s6, s48, 33
	v_mfma_f32_32x32x16_bf16 v[66:81], v[12:15], v[232:235], v[66:81]
	ds_read_b64_tr_b16 v[232:233], v210 offset:0x4200
	ds_read_b64_tr_b16 v[234:235], v210 offset:0x4a00
	v_mfma_f32_32x32x16_bf16 v[66:81], v[178:181], v[236:239], v[66:81]
	ds_read_b64_tr_b16 v[236:237], v210 offset:0x5200
	ds_read_b64_tr_b16 v[238:239], v210 offset:0x5a00
	v_mfma_f32_32x32x16_bf16 v[66:81], v[182:185], v[240:243], v[66:81]
	ds_read_b64_tr_b16 v[240:241], v210 offset:0x6200
	ds_read_b64_tr_b16 v[242:243], v210 offset:0x6a00
	ds_read_b64_tr_b16 v[248:249], v210 offset:0x7200
	ds_read_b64_tr_b16 v[250:251], v210 offset:0x7a00
	s_waitcnt lgkmcnt(0)
	v_mfma_f32_32x32x16_bf16 v[66:81], v[186:189], v[244:247], v[66:81]
	v_mfma_f32_32x32x16_bf16 v[50:65], v[12:15], v[232:235], v[50:65]
	ds_read_b64_tr_b16 v[232:233], v210 offset:0x4400
	ds_read_b64_tr_b16 v[234:235], v210 offset:0x4c00
	v_mfma_f32_32x32x16_bf16 v[50:65], v[178:181], v[236:239], v[50:65]
	ds_read_b64_tr_b16 v[236:237], v210 offset:0x5400
	ds_read_b64_tr_b16 v[238:239], v210 offset:0x5c00
	v_mfma_f32_32x32x16_bf16 v[50:65], v[182:185], v[240:243], v[50:65]
	ds_read_b64_tr_b16 v[240:241], v210 offset:0x6400
	ds_read_b64_tr_b16 v[242:243], v210 offset:0x6c00
	ds_read_b64_tr_b16 v[244:245], v210 offset:0x7400
	ds_read_b64_tr_b16 v[246:247], v210 offset:0x7c00
	s_waitcnt lgkmcnt(0)
	v_mfma_f32_32x32x16_bf16 v[50:65], v[186:189], v[248:251], v[50:65]
	v_mfma_f32_32x32x16_bf16 v[34:49], v[12:15], v[232:235], v[34:49]
	ds_read_b64_tr_b16 v[232:233], v210 offset:0x4600
	ds_read_b64_tr_b16 v[234:235], v210 offset:0x4e00
	v_mfma_f32_32x32x16_bf16 v[34:49], v[178:181], v[236:239], v[34:49]
	ds_read_b64_tr_b16 v[236:237], v210 offset:0x5600
	ds_read_b64_tr_b16 v[238:239], v210 offset:0x5e00
	v_mfma_f32_32x32x16_bf16 v[34:49], v[182:185], v[240:243], v[34:49]
	ds_read_b64_tr_b16 v[240:241], v210 offset:0x6600
	ds_read_b64_tr_b16 v[242:243], v210 offset:0x6e00
	ds_read_b64_tr_b16 v[248:249], v210 offset:0x7600
	ds_read_b64_tr_b16 v[250:251], v210 offset:0x7e00
	s_waitcnt lgkmcnt(0)
	v_mfma_f32_32x32x16_bf16 v[34:49], v[186:189], v[244:247], v[34:49]
	v_mfma_f32_32x32x16_bf16 v[18:33], v[12:15], v[232:235], v[18:33]
	s_cmp_le_i32 s6, s46
	s_cselect_b64 s[6:7], -1, 0
	s_cmp_gt_i32 s10, s18
	s_cselect_b64 s[72:73], -1, 0
	s_and_b64 s[6:7], s[72:73], s[6:7]
	s_and_b64 vcc, exec, s[6:7]
	v_mfma_f32_32x32x16_bf16 v[18:33], v[178:181], v[236:239], v[18:33]
	v_mfma_f32_32x32x16_bf16 v[18:33], v[182:185], v[240:243], v[18:33]
	v_mfma_f32_32x32x16_bf16 v[18:33], v[186:189], v[248:251], v[18:33]
	s_cbranch_vccnz .LBB0_535
	v_add_u32_e32 v12, 59, v193
	v_cmp_gt_u32_e32 vcc, 2.0, v12
	v_add_u32_e32 v12, 27, v193
	s_nop 0
	v_cndmask_b32_e32 v130, v200, v130, vcc
	v_cmp_gt_u32_e32 vcc, 2.0, v12
	v_add_u32_e32 v12, 58, v193
	s_nop 0
	v_cndmask_b32_e32 v114, v200, v114, vcc
	v_cmp_gt_u32_e32 vcc, 2.0, v12
	v_add_u32_e32 v12, 26, v193
	s_nop 0
	v_cndmask_b32_e32 v131, v200, v131, vcc
	v_cmp_gt_u32_e32 vcc, 2.0, v12
	v_add_u32_e32 v12, 57, v193
	s_nop 0
	v_cndmask_b32_e32 v115, v200, v115, vcc
	v_cmp_gt_u32_e32 vcc, 2.0, v12
	v_add_u32_e32 v12, 25, v193
	s_nop 0
	v_cndmask_b32_e32 v132, v200, v132, vcc
	v_cmp_gt_u32_e32 vcc, 2.0, v12
	v_add_u32_e32 v12, 56, v193
	s_nop 0
	v_cndmask_b32_e32 v116, v200, v116, vcc
	v_cmp_gt_u32_e32 vcc, 2.0, v12
	v_add_u32_e32 v12, 24, v193
	s_nop 0
	v_cndmask_b32_e32 v133, v200, v133, vcc
	v_cmp_gt_u32_e32 vcc, 2.0, v12
	v_add_u32_e32 v12, 51, v193
	s_nop 0
	v_cndmask_b32_e32 v117, v200, v117, vcc
	v_cmp_gt_u32_e32 vcc, 2.0, v12
	v_add_u32_e32 v12, 19, v193
	s_nop 0
	v_cndmask_b32_e32 v134, v200, v134, vcc
	v_cmp_gt_u32_e32 vcc, 2.0, v12
	v_add_u32_e32 v12, 50, v193
	s_nop 0
	v_cndmask_b32_e32 v118, v200, v118, vcc
	v_cmp_gt_u32_e32 vcc, 2.0, v12
	v_add_u32_e32 v12, 18, v193
	s_nop 0
	v_cndmask_b32_e32 v135, v200, v135, vcc
	v_cmp_gt_u32_e32 vcc, 2.0, v12
	v_add_u32_e32 v12, 49, v193
	s_nop 0
	v_cndmask_b32_e32 v119, v200, v119, vcc
	v_cmp_gt_u32_e32 vcc, 2.0, v12
	v_add_u32_e32 v12, 17, v193
	s_nop 0
	v_cndmask_b32_e32 v136, v200, v136, vcc
	v_cmp_gt_u32_e32 vcc, 2.0, v12
	v_add_u32_e32 v12, 48, v193
	s_nop 0
	v_cndmask_b32_e32 v120, v200, v120, vcc
	v_cmp_gt_u32_e32 vcc, 2.0, v12
	v_add_u32_e32 v12, 16, v193
	s_nop 0
	v_cndmask_b32_e32 v137, v200, v137, vcc
	v_cmp_gt_u32_e32 vcc, 2.0, v12
	v_add_u32_e32 v12, 43, v193
	s_nop 0
	v_cndmask_b32_e32 v121, v200, v121, vcc
	v_cmp_gt_u32_e32 vcc, 2.0, v12
	v_add_u32_e32 v12, 11, v193
	s_nop 0
	v_cndmask_b32_e32 v138, v200, v138, vcc
	v_cmp_gt_u32_e32 vcc, 2.0, v12
	v_add_u32_e32 v12, 42, v193
	s_nop 0
	v_cndmask_b32_e32 v122, v200, v122, vcc
	v_cmp_gt_u32_e32 vcc, 2.0, v12
	v_add_u32_e32 v12, 10, v193
	s_nop 0
	v_cndmask_b32_e32 v139, v200, v139, vcc
	v_cmp_gt_u32_e32 vcc, 2.0, v12
	v_add_u32_e32 v12, 41, v193
	s_nop 0
	v_cndmask_b32_e32 v123, v200, v123, vcc
	v_cmp_gt_u32_e32 vcc, 2.0, v12
	v_add_u32_e32 v12, 9, v193
	s_nop 0
	v_cndmask_b32_e32 v140, v200, v140, vcc
	v_cmp_gt_u32_e32 vcc, 2.0, v12
	v_add_u32_e32 v12, 40, v193
	s_nop 0
	v_cndmask_b32_e32 v124, v200, v124, vcc
	v_cmp_gt_u32_e32 vcc, 2.0, v12
	v_add_u32_e32 v12, 8, v193
	s_nop 0
	v_cndmask_b32_e32 v141, v200, v141, vcc
	v_cmp_gt_u32_e32 vcc, 2.0, v12
	v_add_u32_e32 v12, 35, v193
	s_nop 0
	v_cndmask_b32_e32 v125, v200, v125, vcc
	v_cmp_gt_u32_e32 vcc, 2.0, v12
	v_add_u32_e32 v12, 3, v193
	s_nop 0
	v_cndmask_b32_e32 v142, v200, v142, vcc
	v_cmp_gt_u32_e32 vcc, 2.0, v12
	v_add_u32_e32 v12, 34, v193
	s_nop 0
	v_cndmask_b32_e32 v126, v200, v126, vcc
	v_cmp_gt_u32_e32 vcc, 2.0, v12
	v_add_u32_e32 v12, 2, v193
	s_nop 0
	v_cndmask_b32_e32 v143, v200, v143, vcc
	v_cmp_gt_u32_e32 vcc, 2.0, v12
	v_add_u32_e32 v12, 33, v193
	s_nop 0
	v_cndmask_b32_e32 v127, v200, v127, vcc
	v_cmp_gt_u32_e32 vcc, 2.0, v12
	v_add_u32_e32 v12, 1, v193
	s_nop 0
	v_cndmask_b32_e32 v144, v200, v144, vcc
	v_cmp_gt_u32_e32 vcc, 2.0, v12
	v_add_u32_e32 v12, 32, v193
	s_nop 0
	v_cndmask_b32_e32 v128, v200, v128, vcc
	v_cmp_gt_u32_e32 vcc, 2.0, v12
	s_nop 1
	v_cndmask_b32_e32 v145, v200, v145, vcc
	v_cmp_gt_u32_e32 vcc, 2.0, v193
	s_nop 1
	v_cndmask_b32_e32 v129, v200, v129, vcc

; __device__ __forceinline__ void finishSM(f32x16& p0, f32x16& p1, float alpha, float& l_reg, bf16x8& pa0, bf16x8& pa1, bf16x8& pa2, bf16x8& pa3) {
; #pragma unroll
;     for (int r = 0; r < 16; ++r) p1[r] = __builtin_amdgcn_exp2f(p1[r]);
;     float ps = 0;
; #pragma unroll
;     for (int r = 0; r < 16; ++r) ps += p0[r];
; #pragma unroll
;     for (int r = 0; r < 16; ++r) ps += p1[r];
;     { auto rr = __builtin_amdgcn_permlane32_swap(__float_as_uint(ps), __float_as_uint(ps), false, false);
;       ps = __uint_as_float(rr[0]) + __uint_as_float(rr[1]); }
;     l_reg = l_reg * alpha + ps;
;     ...
;     PK4(p0, 0, pa0); PK4(p0, 8, pa1); PK4(p1, 0, pa2); PK4(p1, 8, pa3);
; template <int KB, bool SK, bool ROPE, bool QHALF>
; __device__ __forceinline__ void qkt(f32x16& p0, f32x16& p1, const char* lds, int r32, int hi, const bf16x8* qr, const char* qrl, bool act) {
;     ...
;     for (int d0 = 0; d0 < 8; ++d0) { const char* a = kb[d0 & 3] + (d0 >> 2) * 128;
;         bf16x8 b0 = *reinterpret_cast<const bf16x8*>(a);
;         bf16x8 b1 = *reinterpret_cast<const bf16x8*>(a + 32 * 256);
;         bf16x8 qf;
;         if constexpr (QHALF) { if (d0 >= 4) qf = *reinterpret_cast<const bf16x8*>(qrl + (d0 - 4) * 1024); else qf = qr[d0]; } else qf = qr[d0];
;         p0 = __builtin_amdgcn_mfma_f32_32x32x16_bf16(b0, qf, p0, 0, 0, 0);
;         p1 = __builtin_amdgcn_mfma_f32_32x32x16_bf16(b1, qf, p1, 0, 0, 0); }
;     if constexpr (ROPE) {
; #pragma unroll
;         for (int d0 = 0; d0 < 4; ++d0) { const char* a = lds + OFF_KR + KB * SHM_KR + KRSWZ(r32, 2 * d0 + hi);
;             bf16x8 b0 = *reinterpret_cast<const bf16x8*>(a);
;             bf16x8 b1 = *reinterpret_cast<const bf16x8*>(a + 32 * 128);
;             const bf16x8 qf = *reinterpret_cast<const bf16x8*>(qrl + d0 * 1024);
;             p0 = __builtin_amdgcn_mfma_f32_32x32x16_bf16(b0, qf, p0, 0, 0, 0);
;             p1 = __builtin_amdgcn_mfma_f32_32x32x16_bf16(b1, qf, p1, 0, 0, 0); }
.Lmy_nobar_1:
.LBB0_1036:
	ds_read_b128 v[4:7], v212 offset:49152
	ds_read_b128 v[8:11], v212 offset:57344
	s_add_i32 s10, 0, 0x12800
	v_exp_f32_e32 v122, v132
	v_exp_f32_e32 v123, v133
	s_waitcnt lgkmcnt(1)
	v_mfma_f32_32x32x16_bf16 v[102:117], v[4:7], v[174:177], 0
	v_exp_f32_e32 v124, v130
	v_exp_f32_e32 v125, v131
	v_exp_f32_e32 v126, v126
	v_exp_f32_e32 v127, v127
	v_exp_f32_e32 v128, v128
	v_exp_f32_e32 v129, v129
	s_add_i32 s6, s42, 0xffffff60
	s_waitcnt lgkmcnt(0)
	v_mfma_f32_32x32x16_bf16 v[86:101], v[8:11], v[174:177], 0
	ds_read_b128 v[4:7], v213 offset:49152
	ds_read_b128 v[8:11], v213 offset:57344
	s_add_i32 s7, s42, 0xffffff9f
	s_waitcnt lgkmcnt(1)
	v_mfma_f32_32x32x16_bf16 v[102:117], v[4:7], v[170:173], v[102:117]
	s_waitcnt lgkmcnt(0)
	v_mfma_f32_32x32x16_bf16 v[86:101], v[8:11], v[170:173], v[86:101]
	ds_read_b128 v[4:7], v214 offset:49152
	ds_read_b128 v[8:11], v214 offset:57344
	s_waitcnt lgkmcnt(1)
	v_mfma_f32_32x32x16_bf16 v[102:117], v[4:7], v[166:169], v[102:117]
	s_waitcnt lgkmcnt(0)
	v_mfma_f32_32x32x16_bf16 v[86:101], v[8:11], v[166:169], v[86:101]
	ds_read_b128 v[4:7], v215 offset:49152
	ds_read_b128 v[8:11], v215 offset:57344
	s_waitcnt lgkmcnt(1)
	v_mfma_f32_32x32x16_bf16 v[102:117], v[4:7], v[162:165], v[102:117]
	s_waitcnt lgkmcnt(0)
	v_mfma_f32_32x32x16_bf16 v[86:101], v[8:11], v[162:165], v[86:101]
	ds_read_b128 v[4:7], v212 offset:49280
	ds_read_b128 v[8:11], v212 offset:57472
	s_waitcnt lgkmcnt(1)
	v_mfma_f32_32x32x16_bf16 v[102:117], v[4:7], v[158:161], v[102:117]
	s_waitcnt lgkmcnt(0)
	v_mfma_f32_32x32x16_bf16 v[86:101], v[8:11], v[158:161], v[86:101]
	ds_read_b128 v[4:7], v213 offset:49280
	ds_read_b128 v[8:11], v213 offset:57472
	s_waitcnt lgkmcnt(1)
	v_mfma_f32_32x32x16_bf16 v[102:117], v[4:7], v[154:157], v[102:117]
	s_waitcnt lgkmcnt(0)
	v_mfma_f32_32x32x16_bf16 v[86:101], v[8:11], v[154:157], v[86:101]
	ds_read_b128 v[4:7], v214 offset:49280
	ds_read_b128 v[8:11], v214 offset:57472
	s_waitcnt lgkmcnt(1)
	v_mfma_f32_32x32x16_bf16 v[102:117], v[4:7], v[150:153], v[102:117]
	s_waitcnt lgkmcnt(0)
	v_mfma_f32_32x32x16_bf16 v[86:101], v[8:11], v[150:153], v[86:101]
	ds_read_b128 v[4:7], v215 offset:49280
	ds_read_b128 v[8:11], v215 offset:57472
	s_waitcnt lgkmcnt(1)
	v_mfma_f32_32x32x16_bf16 v[102:117], v[4:7], v[146:149], v[102:117]
	s_waitcnt lgkmcnt(0)
	v_mfma_f32_32x32x16_bf16 v[86:101], v[8:11], v[146:149], v[86:101]
	v_add_u32_e32 v8, s10, v216
	ds_read_b128 v[4:7], v8
	ds_read_b128 v[8:11], v8 offset:4096
	ds_read_b128 v[12:15], v202
	s_waitcnt lgkmcnt(0)
	v_mfma_f32_32x32x16_bf16 v[102:117], v[4:7], v[12:15], v[102:117]
	v_mfma_f32_32x32x16_bf16 v[86:101], v[8:11], v[12:15], v[86:101]
	v_add_u32_e32 v8, s10, v217
	ds_read_b128 v[4:7], v8
	ds_read_b128 v[8:11], v8 offset:4096
	ds_read_b128 v[12:15], v202 offset:1024
	s_waitcnt lgkmcnt(0)
	v_mfma_f32_32x32x16_bf16 v[102:117], v[4:7], v[12:15], v[102:117]
	v_mfma_f32_32x32x16_bf16 v[86:101], v[8:11], v[12:15], v[86:101]
	v_add_u32_e32 v8, s10, v218
	ds_read_b128 v[4:7], v8
	ds_read_b128 v[8:11], v8 offset:4096
	ds_read_b128 v[12:15], v202 offset:2048
	s_waitcnt lgkmcnt(0)
	v_mfma_f32_32x32x16_bf16 v[102:117], v[4:7], v[12:15], v[102:117]
	v_mfma_f32_32x32x16_bf16 v[86:101], v[8:11], v[12:15], v[86:101]
	v_add_u32_e32 v8, s10, v219
	ds_read_b128 v[4:7], v8
	ds_read_b128 v[8:11], v8 offset:4096
	ds_read_b128 v[12:15], v202 offset:3072
	s_waitcnt lgkmcnt(0)
	v_mfma_f32_32x32x16_bf16 v[102:117], v[4:7], v[12:15], v[102:117]
	v_exp_f32_e32 v4, v140
	v_exp_f32_e32 v5, v141
	v_exp_f32_e32 v6, v138
	v_exp_f32_e32 v7, v139
	v_mfma_f32_32x32x16_bf16 v[86:101], v[8:11], v[12:15], v[86:101]
	ds_read_b64_tr_b16 v[230:231], v209 offset:0
	ds_read_b64_tr_b16 v[232:233], v209 offset:0x800
	ds_read_b64_tr_b16 v[234:235], v209 offset:0x1000
	ds_read_b64_tr_b16 v[236:237], v209 offset:0x1800
	ds_read_b64_tr_b16 v[238:239], v209 offset:0x2000
	ds_read_b64_tr_b16 v[240:241], v209 offset:0x2800
	ds_read_b64_tr_b16 v[242:243], v209 offset:0x3000
	ds_read_b64_tr_b16 v[244:245], v209 offset:0x3800
	v_add_f32_e32 v12, 0, v188
	v_add_f32_e32 v12, v227, v12
	v_add_f32_e32 v12, v186, v12
	v_add_f32_e32 v12, v189, v12
	v_add_f32_e32 v12, v185, v12
	v_add_f32_e32 v12, v187, v12
	v_add_f32_e32 v12, v183, v12
	v_add_f32_e32 v12, v184, v12
	v_add_f32_e32 v12, v179, v12
	v_add_f32_e32 v12, v182, v12
	v_add_f32_e32 v12, v144, v12
	v_add_f32_e32 v12, v180, v12
	v_add_f32_e32 v12, v142, v12
	v_add_f32_e32 v12, v181, v12
	v_add_f32_e32 v12, v143, v12
	v_add_f32_e32 v12, v145, v12
	v_exp_f32_e32 v8, v136
	v_add_f32_e32 v12, v4, v12
	v_exp_f32_e32 v9, v137
	v_add_f32_e32 v12, v5, v12
	v_exp_f32_e32 v10, v134
	v_add_f32_e32 v12, v6, v12
	v_exp_f32_e32 v11, v135
	v_add_f32_e32 v12, v7, v12
	v_add_f32_e32 v12, v8, v12
	v_add_f32_e32 v12, v9, v12
	v_add_f32_e32 v12, v10, v12
	v_add_f32_e32 v12, v11, v12
	v_add_f32_e32 v12, v122, v12
	v_add_f32_e32 v12, v123, v12
	v_add_f32_e32 v12, v124, v12
	v_add_f32_e32 v12, v125, v12
	v_add_f32_e32 v12, v126, v12
	v_add_f32_e32 v12, v127, v12
	v_add_f32_e32 v12, v128, v12
	v_add_f32_e32 v195, v129, v12
	v_mov_b32_e32 v225, v195
	s_nop 1
	v_permlane32_swap_b32_e32 v195, v225
	v_cvt_pk_bf16_f32 v12, v188, v227
	v_cvt_pk_bf16_f32 v13, v186, v189
	v_cvt_pk_bf16_f32 v14, v185, v187
	v_cvt_pk_bf16_f32 v15, v183, v184
	v_cvt_pk_bf16_f32 v82, v179, v182
	v_cvt_pk_bf16_f32 v83, v144, v180
	v_cvt_pk_bf16_f32 v84, v142, v181
	v_cvt_pk_bf16_f32 v85, v143, v145
	v_cvt_pk_bf16_f32 v118, v4, v5
	v_cvt_pk_bf16_f32 v119, v6, v7
	v_cvt_pk_bf16_f32 v120, v8, v9
	v_cvt_pk_bf16_f32 v121, v10, v11
	v_cvt_pk_bf16_f32 v122, v122, v123
	v_cvt_pk_bf16_f32 v123, v124, v125
	v_cvt_pk_bf16_f32 v124, v126, v127
	v_cvt_pk_bf16_f32 v125, v128, v129
	s_nop 0
	v_permlane32_swap_b32_e32 v12, v14
	v_permlane32_swap_b32_e32 v13, v15
	v_permlane32_swap_b32_e32 v82, v84
	v_permlane32_swap_b32_e32 v83, v85
	v_permlane32_swap_b32_e32 v118, v120
	v_permlane32_swap_b32_e32 v119, v121
	v_permlane32_swap_b32_e32 v122, v124
	v_permlane32_swap_b32_e32 v123, v125
	s_add_i32 s10, s42, 0xffffffa0
	s_sub_i32 s64, s42, 64
	s_mov_b32 s65, s11
	s_lshl_b64 s[44:45], s[10:11], 12
	s_lshl_b64 s[64:65], s[64:65], 12
	v_lshl_add_u64 v[4:5], v[196:197], 0, s[44:45]
	v_lshl_add_u64 v[8:9], v[196:197], 0, s[64:65]
	v_lshl_add_u64 v[126:127], v[198:199], 0, s[44:45]
	s_add_i32 m0, s37, 0x8000
	global_load_dwordx4 v[4:7], v[4:5], off
	s_nop 0
	global_load_dwordx4 v[8:11], v[8:9], off
	s_lshl_b64 s[44:45], s[10:11], 7
	global_load_lds_dwordx4 v[126:127], off
	v_lshl_add_u64 v[126:127], v[198:199], 0, s[64:65]
	s_add_i32 m0, s37, 0xa000
	s_nop 0
	global_load_lds_dwordx4 v[126:127], off
	v_lshl_add_u64 v[126:127], v[16:17], 0, s[44:45]
	s_add_i32 m0, s37, 0x10800
	s_nop 0
	global_load_lds_dwordx4 v[126:127], off
	s_waitcnt lgkmcnt(0)
; __device__ __forceinline__ void mask_tile(f32x16& p0, f32x16& p1, int dq, unsigned W) {
;     const float NEG = -__builtin_inff();
; #pragma unroll
;     for (int r = 0; r < 16; ++r) {
;         const int c = (r & 3) + 8 * (r >> 2);
;         if ((unsigned)(dq - c) >= W) p0[r] = NEG;
;         if ((unsigned)(dq - c - 32) >= W) p1[r] = NEG;
;     }
; }
; template <int VB, bool SK>
; __device__ __forceinline__ void pv_tile(f32x16* o, int vb0, bf16x8 pa0, bf16x8 pa1, bf16x8 pa2, bf16x8 pa3, bool act) {
;     if (SK && !act) return;
;     ...
;     if (ATT_PRIO) __builtin_amdgcn_s_setprio(1);
;     PV_D0(0); PV_D0(1); PV_D0(2); PV_D0(3);
	s_nop 0
	v_mfma_f32_32x32x16_bf16 v[66:81], v[12:15], v[230:233], v[66:81]
	ds_read_b64_tr_b16 v[126:127], v209 offset:0x200
	ds_read_b64_tr_b16 v[128:129], v209 offset:0xa00
	v_mfma_f32_32x32x16_bf16 v[66:81], v[82:85], v[234:237], v[66:81]
	ds_read_b64_tr_b16 v[130:131], v209 offset:0x1200
	ds_read_b64_tr_b16 v[132:133], v209 offset:0x1a00
	v_mfma_f32_32x32x16_bf16 v[66:81], v[118:121], v[238:241], v[66:81]
	ds_read_b64_tr_b16 v[134:135], v209 offset:0x2200
	ds_read_b64_tr_b16 v[136:137], v209 offset:0x2a00
	ds_read_b64_tr_b16 v[142:143], v209 offset:0x3200
	ds_read_b64_tr_b16 v[144:145], v209 offset:0x3a00
	s_waitcnt lgkmcnt(0)
	v_mfma_f32_32x32x16_bf16 v[66:81], v[122:125], v[242:245], v[66:81]
	v_mfma_f32_32x32x16_bf16 v[50:65], v[12:15], v[126:129], v[50:65]
	ds_read_b64_tr_b16 v[126:127], v209 offset:0x400
	ds_read_b64_tr_b16 v[128:129], v209 offset:0xc00
	v_mfma_f32_32x32x16_bf16 v[50:65], v[82:85], v[130:133], v[50:65]
	ds_read_b64_tr_b16 v[130:131], v209 offset:0x1400
	ds_read_b64_tr_b16 v[132:133], v209 offset:0x1c00
	v_mfma_f32_32x32x16_bf16 v[50:65], v[118:121], v[134:137], v[50:65]
	ds_read_b64_tr_b16 v[134:135], v209 offset:0x2400
	ds_read_b64_tr_b16 v[136:137], v209 offset:0x2c00
	ds_read_b64_tr_b16 v[138:139], v209 offset:0x3400
	ds_read_b64_tr_b16 v[140:141], v209 offset:0x3c00
	s_waitcnt lgkmcnt(0)
	v_mfma_f32_32x32x16_bf16 v[50:65], v[122:125], v[142:145], v[50:65]
	v_mfma_f32_32x32x16_bf16 v[34:49], v[12:15], v[126:129], v[34:49]
	ds_read_b64_tr_b16 v[126:127], v209 offset:0x600
	ds_read_b64_tr_b16 v[128:129], v209 offset:0xe00
	v_mfma_f32_32x32x16_bf16 v[34:49], v[82:85], v[130:133], v[34:49]
	ds_read_b64_tr_b16 v[130:131], v209 offset:0x1600
	ds_read_b64_tr_b16 v[132:133], v209 offset:0x1e00
	v_mfma_f32_32x32x16_bf16 v[34:49], v[118:121], v[134:137], v[34:49]
	ds_read_b64_tr_b16 v[134:135], v209 offset:0x2600
	ds_read_b64_tr_b16 v[136:137], v209 offset:0x2e00
	ds_read_b64_tr_b16 v[142:143], v209 offset:0x3600
	ds_read_b64_tr_b16 v[144:145], v209 offset:0x3e00
	s_waitcnt lgkmcnt(0)
	v_mfma_f32_32x32x16_bf16 v[34:49], v[122:125], v[138:141], v[34:49]
	v_mfma_f32_32x32x16_bf16 v[18:33], v[12:15], v[126:129], v[18:33]
	s_cmp_le_i32 s7, s40
	s_cselect_b64 s[44:45], -1, 0
	s_cmp_gt_i32 s6, s60
	s_cselect_b64 s[6:7], -1, 0
	s_and_b64 s[6:7], s[6:7], s[44:45]
	s_and_b64 vcc, exec, s[6:7]
	v_mfma_f32_32x32x16_bf16 v[18:33], v[82:85], v[130:133], v[18:33]
	v_mfma_f32_32x32x16_bf16 v[18:33], v[118:121], v[134:137], v[18:33]
	v_mfma_f32_32x32x16_bf16 v[18:33], v[122:125], v[142:145], v[18:33]
	s_cbranch_vccnz .LBB0_1038
	v_add_u32_e32 v12, 0x7b, v193
	v_cmp_gt_u32_e32 vcc, 2.0, v12
	v_add_u32_e32 v12, 0x5b, v193
	s_nop 0
	v_cndmask_b32_e32 v102, v200, v102, vcc
	v_cmp_gt_u32_e32 vcc, 2.0, v12
	v_add_u32_e32 v12, 0x7a, v193
	s_nop 0
	v_cndmask_b32_e32 v86, v200, v86, vcc
	v_cmp_gt_u32_e32 vcc, 2.0, v12
	v_add_u32_e32 v12, 0x5a, v193
	s_nop 0
	v_cndmask_b32_e32 v103, v200, v103, vcc
	v_cmp_gt_u32_e32 vcc, 2.0, v12
	v_add_u32_e32 v12, 0x79, v193
	s_nop 0
	v_cndmask_b32_e32 v87, v200, v87, vcc
	v_cmp_gt_u32_e32 vcc, 2.0, v12
	v_add_u32_e32 v12, 0x59, v193
	s_nop 0
	v_cndmask_b32_e32 v104, v200, v104, vcc
	v_cmp_gt_u32_e32 vcc, 2.0, v12
	v_add_u32_e32 v12, 0x78, v193
	s_nop 0
	v_cndmask_b32_e32 v88, v200, v88, vcc
	v_cmp_gt_u32_e32 vcc, 2.0, v12
	v_add_u32_e32 v12, 0x58, v193
	s_nop 0
	v_cndmask_b32_e32 v105, v200, v105, vcc
	v_cmp_gt_u32_e32 vcc, 2.0, v12
	v_add_u32_e32 v12, 0x73, v193
	s_nop 0
	v_cndmask_b32_e32 v89, v200, v89, vcc
	v_cmp_gt_u32_e32 vcc, 2.0, v12
	v_add_u32_e32 v12, 0x53, v193
	s_nop 0
	v_cndmask_b32_e32 v106, v200, v106, vcc
	v_cmp_gt_u32_e32 vcc, 2.0, v12
	v_add_u32_e32 v12, 0x72, v193
	s_nop 0
	v_cndmask_b32_e32 v90, v200, v90, vcc
	v_cmp_gt_u32_e32 vcc, 2.0, v12
	v_add_u32_e32 v12, 0x52, v193
	s_nop 0
	v_cndmask_b32_e32 v107, v200, v107, vcc
	v_cmp_gt_u32_e32 vcc, 2.0, v12
	v_add_u32_e32 v12, 0x71, v193
	s_nop 0
	v_cndmask_b32_e32 v91, v200, v91, vcc
	v_cmp_gt_u32_e32 vcc, 2.0, v12
	v_add_u32_e32 v12, 0x51, v193
	s_nop 0
	v_cndmask_b32_e32 v108, v200, v108, vcc
	v_cmp_gt_u32_e32 vcc, 2.0, v12
	v_add_u32_e32 v12, 0x70, v193
	s_nop 0
	v_cndmask_b32_e32 v92, v200, v92, vcc
	v_cmp_gt_u32_e32 vcc, 2.0, v12
	v_add_u32_e32 v12, 0x50, v193
	s_nop 0
	v_cndmask_b32_e32 v109, v200, v109, vcc
	v_cmp_gt_u32_e32 vcc, 2.0, v12
	v_add_u32_e32 v12, 0x6b, v193
	s_nop 0
	v_cndmask_b32_e32 v93, v200, v93, vcc
	v_cmp_gt_u32_e32 vcc, 2.0, v12
	v_add_u32_e32 v12, 0x4b, v193
	s_nop 0
	v_cndmask_b32_e32 v110, v200, v110, vcc
	v_cmp_gt_u32_e32 vcc, 2.0, v12
	v_add_u32_e32 v12, 0x6a, v193
	s_nop 0
	v_cndmask_b32_e32 v94, v200, v94, vcc
	v_cmp_gt_u32_e32 vcc, 2.0, v12
	v_add_u32_e32 v12, 0x4a, v193
	s_nop 0
	v_cndmask_b32_e32 v111, v200, v111, vcc
	v_cmp_gt_u32_e32 vcc, 2.0, v12
	v_add_u32_e32 v12, 0x69, v193
	s_nop 0
	v_cndmask_b32_e32 v95, v200, v95, vcc
	v_cmp_gt_u32_e32 vcc, 2.0, v12
	v_add_u32_e32 v12, 0x49, v193
	s_nop 0
	v_cndmask_b32_e32 v112, v200, v112, vcc
	v_cmp_gt_u32_e32 vcc, 2.0, v12
	v_add_u32_e32 v12, 0x68, v193
	s_nop 0
	v_cndmask_b32_e32 v96, v200, v96, vcc
	v_cmp_gt_u32_e32 vcc, 2.0, v12
	v_add_u32_e32 v12, 0x48, v193
	s_nop 0
	v_cndmask_b32_e32 v113, v200, v113, vcc
	v_cmp_gt_u32_e32 vcc, 2.0, v12
	v_add_u32_e32 v12, 0x63, v193
	s_nop 0
	v_cndmask_b32_e32 v97, v200, v97, vcc
	v_cmp_gt_u32_e32 vcc, 2.0, v12
	v_add_u32_e32 v12, 0x43, v193
	s_nop 0
	v_cndmask_b32_e32 v114, v200, v114, vcc
	v_cmp_gt_u32_e32 vcc, 2.0, v12
	v_add_u32_e32 v12, 0x62, v193
	s_nop 0
	v_cndmask_b32_e32 v98, v200, v98, vcc
	v_cmp_gt_u32_e32 vcc, 2.0, v12
	v_add_u32_e32 v12, 0x42, v193
	s_nop 0
	v_cndmask_b32_e32 v115, v200, v115, vcc
	v_cmp_gt_u32_e32 vcc, 2.0, v12
	v_add_u32_e32 v12, 0x61, v193
	s_nop 0
	v_cndmask_b32_e32 v99, v200, v99, vcc
	v_cmp_gt_u32_e32 vcc, 2.0, v12
	v_add_u32_e32 v12, 0x41, v193
	s_nop 0
	v_cndmask_b32_e32 v116, v200, v116, vcc
	v_cmp_gt_u32_e32 vcc, 2.0, v12
	v_add_u32_e32 v12, 0x60, v193
	s_nop 0
	v_cndmask_b32_e32 v100, v200, v100, vcc
	v_cmp_gt_u32_e32 vcc, 2.0, v12
	v_add_u32_e32 v12, 64, v193
	s_nop 0
	v_cndmask_b32_e32 v117, v200, v117, vcc
	v_cmp_gt_u32_e32 vcc, 2.0, v12
	s_nop 1
	v_cndmask_b32_e32 v101, v200, v101, vcc

; template <int MODE>
; __device__ __forceinline__ void partialSM(f32x16& p0, f32x16& p1, float& m_reg, float& mn, float& alpha) {
;     ...
;     constexpr float C2 = 1.4426950408889634f * SCALE;
;     if (__builtin_expect(__all((pmax - m_reg) * SCALE <= THR), 1)) { mn = m_reg; alpha = 1.f; }
;     else { mn = fmaxf(m_reg, pmax); alpha = __builtin_amdgcn_exp2f((m_reg - mn) * C2); m_reg = mn; }
;     const float mnL = -mn * C2;
; #pragma unroll
;     for (int r = 0; r < 16; ++r) p0[r] = fmaf(p0[r], C2, mnL);
; #pragma unroll
;     for (int r = 0; r < 16; ++r) p1[r] = fmaf(p1[r], C2, mnL);
; #pragma unroll
;     for (int r = 0; r < 16; ++r) p0[r] = __builtin_amdgcn_exp2f(p0[r]);
; template <int KB, bool SK, bool ROPE, bool QHALF>
; __device__ __forceinline__ void qkt(f32x16& p0, f32x16& p1, const char* lds, int r32, int hi, const bf16x8* qr, const char* qrl, bool act) {
;     ...
;     for (int d0 = 0; d0 < 8; ++d0) { const char* a = kb[d0 & 3] + (d0 >> 2) * 128;
;         bf16x8 b0 = *reinterpret_cast<const bf16x8*>(a);
;         bf16x8 b1 = *reinterpret_cast<const bf16x8*>(a + 32 * 256);
;         bf16x8 qf;
;         if constexpr (QHALF) { if (d0 >= 4) qf = *reinterpret_cast<const bf16x8*>(qrl + (d0 - 4) * 1024); else qf = qr[d0]; } else qf = qr[d0];
;         p0 = __builtin_amdgcn_mfma_f32_32x32x16_bf16(b0, qf, p0, 0, 0, 0);
;         p1 = __builtin_amdgcn_mfma_f32_32x32x16_bf16(b1, qf, p1, 0, 0, 0); }
;     if constexpr (ROPE) {
; #pragma unroll
;         for (int d0 = 0; d0 < 4; ++d0) { const char* a = lds + OFF_KR + KB * SHM_KR + KRSWZ(r32, 2 * d0 + hi);
;             bf16x8 b0 = *reinterpret_cast<const bf16x8*>(a);
;             bf16x8 b1 = *reinterpret_cast<const bf16x8*>(a + 32 * 128);
;             const bf16x8 qf = *reinterpret_cast<const bf16x8*>(qrl + d0 * 1024);
;             p0 = __builtin_amdgcn_mfma_f32_32x32x16_bf16(b0, qf, p0, 0, 0, 0);
;             p1 = __builtin_amdgcn_mfma_f32_32x32x16_bf16(b1, qf, p1, 0, 0, 0); }
.LBB0_1042:
	v_cndmask_b32_e64 v227, v12, v178, s[6:7]
	v_mul_f32_e32 v12, 0xbdd53b94, v227
	v_fmamk_f32 v82, v102, 0x3dd53b94, v12
	v_fmamk_f32 v83, v103, 0x3dd53b94, v12
	v_fmamk_f32 v84, v104, 0x3dd53b94, v12
	v_fmamk_f32 v85, v105, 0x3dd53b94, v12
	v_fmamk_f32 v118, v106, 0x3dd53b94, v12
	v_fmamk_f32 v119, v107, 0x3dd53b94, v12
	v_fmamk_f32 v120, v108, 0x3dd53b94, v12
	v_fmamk_f32 v121, v109, 0x3dd53b94, v12
	v_fmamk_f32 v122, v110, 0x3dd53b94, v12
	v_fmamk_f32 v123, v111, 0x3dd53b94, v12
	v_fmamk_f32 v112, v112, 0x3dd53b94, v12
	v_fmamk_f32 v113, v113, 0x3dd53b94, v12
	v_fmamk_f32 v114, v114, 0x3dd53b94, v12
	v_fmamk_f32 v115, v115, 0x3dd53b94, v12
	v_fmamk_f32 v116, v116, 0x3dd53b94, v12
	v_fmamk_f32 v117, v117, 0x3dd53b94, v12
	v_fmamk_f32 v102, v86, 0x3dd53b94, v12
	v_fmamk_f32 v103, v87, 0x3dd53b94, v12
	v_fmamk_f32 v104, v88, 0x3dd53b94, v12
	v_fmamk_f32 v110, v89, 0x3dd53b94, v12
	v_fmamk_f32 v111, v90, 0x3dd53b94, v12
	v_fmamk_f32 v14, v91, 0x3dd53b94, v12
	v_fmamk_f32 v15, v92, 0x3dd53b94, v12
	v_fmamk_f32 v105, v93, 0x3dd53b94, v12
	v_fmamk_f32 v106, v94, 0x3dd53b94, v12
	v_fmamk_f32 v107, v95, 0x3dd53b94, v12
	v_fmamk_f32 v108, v96, 0x3dd53b94, v12
	v_fmamk_f32 v109, v97, 0x3dd53b94, v12
	v_exp_f32_e32 v82, v82
	v_exp_f32_e32 v83, v83
	v_exp_f32_e32 v84, v84
	v_exp_f32_e32 v85, v85
	v_exp_f32_e32 v86, v118
	v_exp_f32_e32 v87, v119
	v_exp_f32_e32 v88, v120
	v_exp_f32_e32 v89, v121
	v_exp_f32_e32 v90, v122
	v_exp_f32_e32 v91, v123
	v_exp_f32_e32 v92, v112
	v_exp_f32_e32 v93, v113
	v_exp_f32_e32 v94, v114
	v_exp_f32_e32 v95, v115
	v_exp_f32_e32 v96, v116
	v_exp_f32_e32 v97, v117
	v_fmamk_f32 v13, v98, 0x3dd53b94, v12
	v_fmamk_f32 v112, v99, 0x3dd53b94, v12
	v_fmamk_f32 v113, v100, 0x3dd53b94, v12
	v_fmac_f32_e32 v12, 0x3dd53b94, v101
	s_waitcnt lgkmcnt(0)
	ds_read_b128 v[98:101], v212 offset:32768
	ds_read_b128 v[114:117], v212 offset:40960
	v_exp_f32_e32 v105, v105
	v_exp_f32_e32 v106, v106
	v_exp_f32_e32 v107, v107
	s_waitcnt lgkmcnt(1)
	v_mfma_f32_32x32x16_bf16 v[130:145], v[98:101], v[174:177], 0
	ds_read_b128 v[98:101], v213 offset:32768
	ds_read_b128 v[178:181], v213 offset:40960
	v_exp_f32_e32 v108, v108
	v_exp_f32_e32 v109, v109
	s_waitcnt lgkmcnt(2)
	v_mfma_f32_32x32x16_bf16 v[114:129], v[114:117], v[174:177], 0
	s_waitcnt lgkmcnt(1)
	v_mfma_f32_32x32x16_bf16 v[130:145], v[98:101], v[170:173], v[130:145]
	s_waitcnt lgkmcnt(0)
	v_mfma_f32_32x32x16_bf16 v[114:129], v[178:181], v[170:173], v[114:129]
	ds_read_b128 v[98:101], v214 offset:32768
	ds_read_b128 v[178:181], v214 offset:40960
	s_waitcnt lgkmcnt(1)
	v_mfma_f32_32x32x16_bf16 v[130:145], v[98:101], v[166:169], v[130:145]
	s_waitcnt lgkmcnt(0)
	v_mfma_f32_32x32x16_bf16 v[114:129], v[178:181], v[166:169], v[114:129]
	ds_read_b128 v[98:101], v215 offset:32768
	ds_read_b128 v[178:181], v215 offset:40960
	s_waitcnt lgkmcnt(1)
	v_mfma_f32_32x32x16_bf16 v[130:145], v[98:101], v[162:165], v[130:145]
	s_waitcnt lgkmcnt(0)
	v_mfma_f32_32x32x16_bf16 v[114:129], v[178:181], v[162:165], v[114:129]
	ds_read_b128 v[98:101], v212 offset:32896
	ds_read_b128 v[178:181], v212 offset:41088
	s_waitcnt lgkmcnt(1)
	v_mfma_f32_32x32x16_bf16 v[130:145], v[98:101], v[158:161], v[130:145]
	s_waitcnt lgkmcnt(0)
	v_mfma_f32_32x32x16_bf16 v[114:129], v[178:181], v[158:161], v[114:129]
	ds_read_b128 v[98:101], v213 offset:32896
	ds_read_b128 v[178:181], v213 offset:41088
	s_waitcnt lgkmcnt(1)
	v_mfma_f32_32x32x16_bf16 v[130:145], v[98:101], v[154:157], v[130:145]
	s_waitcnt lgkmcnt(0)
	v_mfma_f32_32x32x16_bf16 v[114:129], v[178:181], v[154:157], v[114:129]
	ds_read_b128 v[98:101], v214 offset:32896
	ds_read_b128 v[178:181], v214 offset:41088
	s_waitcnt lgkmcnt(1)
	v_mfma_f32_32x32x16_bf16 v[130:145], v[98:101], v[150:153], v[130:145]
	s_waitcnt lgkmcnt(0)
	v_mfma_f32_32x32x16_bf16 v[114:129], v[178:181], v[150:153], v[114:129]
	ds_read_b128 v[98:101], v215 offset:32896
	ds_read_b128 v[178:181], v215 offset:41088
	s_waitcnt lgkmcnt(1)
	v_mfma_f32_32x32x16_bf16 v[130:145], v[98:101], v[146:149], v[130:145]
	s_waitcnt lgkmcnt(0)
	v_mfma_f32_32x32x16_bf16 v[114:129], v[178:181], v[146:149], v[114:129]
	ds_read_b128 v[98:101], v221
	ds_read_b128 v[178:181], v221 offset:4096
	ds_read_b128 v[182:185], v202
	s_waitcnt lgkmcnt(0)
	v_mfma_f32_32x32x16_bf16 v[130:145], v[98:101], v[182:185], v[130:145]
	v_mfma_f32_32x32x16_bf16 v[114:129], v[178:181], v[182:185], v[114:129]
	ds_read_b128 v[98:101], v222
	ds_read_b128 v[178:181], v222 offset:4096
	ds_read_b128 v[182:185], v202 offset:1024
	s_waitcnt lgkmcnt(0)
	v_mfma_f32_32x32x16_bf16 v[130:145], v[98:101], v[182:185], v[130:145]
	v_mfma_f32_32x32x16_bf16 v[114:129], v[178:181], v[182:185], v[114:129]
	ds_read_b128 v[98:101], v223
	ds_read_b128 v[178:181], v223 offset:4096
	ds_read_b128 v[182:185], v202 offset:2048
	s_waitcnt lgkmcnt(0)
	v_mfma_f32_32x32x16_bf16 v[130:145], v[98:101], v[182:185], v[130:145]
	v_mfma_f32_32x32x16_bf16 v[114:129], v[178:181], v[182:185], v[114:129]
	ds_read_b128 v[98:101], v224
	ds_read_b128 v[178:181], v224 offset:4096
	ds_read_b128 v[182:185], v202 offset:3072
	s_waitcnt lgkmcnt(0)
; __device__ __forceinline__ void finishSM(f32x16& p0, f32x16& p1, float alpha, float& l_reg, bf16x8& pa0, bf16x8& pa1, bf16x8& pa2, bf16x8& pa3) {
; #pragma unroll
;     for (int r = 0; r < 16; ++r) p1[r] = __builtin_amdgcn_exp2f(p1[r]);
;     float ps = 0;
; #pragma unroll
;     for (int r = 0; r < 16; ++r) ps += p0[r];
; #pragma unroll
;     for (int r = 0; r < 16; ++r) ps += p1[r];
;     { auto rr = __builtin_amdgcn_permlane32_swap(__float_as_uint(ps), __float_as_uint(ps), false, false);
;       ps = __uint_as_float(rr[0]) + __uint_as_float(rr[1]); }
;     l_reg = l_reg * alpha + ps;
;     ...
;     PK4(p0, 0, pa0); PK4(p0, 8, pa1); PK4(p1, 0, pa2); PK4(p1, 8, pa3);
	v_mfma_f32_32x32x16_bf16 v[130:145], v[98:101], v[182:185], v[130:145]
	ds_read_b64_tr_b16 v[230:231], v209 offset:0x4000
	ds_read_b64_tr_b16 v[232:233], v209 offset:0x4800
	ds_read_b64_tr_b16 v[234:235], v209 offset:0x5000
	ds_read_b64_tr_b16 v[236:237], v209 offset:0x5800
	ds_read_b64_tr_b16 v[238:239], v209 offset:0x6000
	ds_read_b64_tr_b16 v[240:241], v209 offset:0x6800
	ds_read_b64_tr_b16 v[242:243], v209 offset:0x7000
	ds_read_b64_tr_b16 v[244:245], v209 offset:0x7800
	v_exp_f32_e32 v98, v102
	v_exp_f32_e32 v102, v111
	v_exp_f32_e32 v111, v112
	v_exp_f32_e32 v112, v113
	v_exp_f32_e32 v113, v12
	v_add_f32_e32 v12, 0, v82
	v_add_f32_e32 v12, v83, v12
	v_add_f32_e32 v12, v84, v12
	v_add_f32_e32 v12, v85, v12
	v_add_f32_e32 v12, v86, v12
	v_add_f32_e32 v12, v87, v12
	v_add_f32_e32 v12, v88, v12
	v_add_f32_e32 v12, v89, v12
	v_add_f32_e32 v12, v90, v12
	v_add_f32_e32 v12, v91, v12
	v_add_f32_e32 v12, v92, v12
	v_add_f32_e32 v12, v93, v12
	v_add_f32_e32 v12, v94, v12
	v_exp_f32_e32 v99, v103
	v_add_f32_e32 v12, v95, v12
	v_exp_f32_e32 v100, v104
	v_add_f32_e32 v12, v96, v12
	v_exp_f32_e32 v101, v110
	v_add_f32_e32 v12, v97, v12
	v_add_f32_e32 v12, v98, v12
	v_exp_f32_e32 v103, v14
	v_add_f32_e32 v12, v99, v12
	v_exp_f32_e32 v104, v15
	v_add_f32_e32 v12, v100, v12
	v_add_f32_e32 v12, v101, v12
	v_add_f32_e32 v12, v102, v12
	v_add_f32_e32 v12, v103, v12
	v_add_f32_e32 v12, v104, v12
	v_add_f32_e32 v12, v105, v12
	v_exp_f32_e32 v110, v13
	v_add_f32_e32 v12, v106, v12
	v_add_f32_e32 v12, v107, v12
	v_mfma_f32_32x32x16_bf16 v[114:129], v[178:181], v[182:185], v[114:129]
	v_add_f32_e32 v12, v108, v12
	v_add_f32_e32 v12, v109, v12
	v_add_f32_e32 v12, v110, v12
	v_add_f32_e32 v12, v111, v12
	v_add_f32_e32 v12, v112, v12
	v_add_f32_e32 v228, v113, v12
	v_mov_b32_e32 v229, v228
	v_cvt_pk_bf16_f32 v12, v82, v83
	v_cvt_pk_bf16_f32 v13, v84, v85
	v_cvt_pk_bf16_f32 v14, v86, v87
	v_cvt_pk_bf16_f32 v15, v88, v89
	v_cvt_pk_bf16_f32 v178, v90, v91
	v_cvt_pk_bf16_f32 v179, v92, v93
	v_cvt_pk_bf16_f32 v180, v94, v95
	v_cvt_pk_bf16_f32 v181, v96, v97
	v_cvt_pk_bf16_f32 v182, v98, v99
	v_cvt_pk_bf16_f32 v183, v100, v101
	v_cvt_pk_bf16_f32 v184, v102, v103
	v_cvt_pk_bf16_f32 v185, v104, v105
	v_cvt_pk_bf16_f32 v186, v106, v107
	v_cvt_pk_bf16_f32 v187, v108, v109
	v_cvt_pk_bf16_f32 v188, v110, v111
	v_cvt_pk_bf16_f32 v189, v112, v113
	s_nop 1
	v_permlane32_swap_b32_e32 v228, v229
	v_permlane32_swap_b32_e32 v12, v14
	v_permlane32_swap_b32_e32 v13, v15
	v_permlane32_swap_b32_e32 v178, v180
	v_permlane32_swap_b32_e32 v179, v181
	v_permlane32_swap_b32_e32 v182, v184
	v_permlane32_swap_b32_e32 v183, v185
	v_permlane32_swap_b32_e32 v186, v188
	v_permlane32_swap_b32_e32 v187, v189
	s_add_i32 s6, s36, 1
	s_cmp_lt_i32 s6, s63
	s_cselect_b64 s[44:45], -1, 0
	s_cmp_ge_i32 s6, s63
	s_cbranch_scc1 .LBB0_1044
	s_sub_i32 s6, s42, 32
	s_mov_b32 s7, s11
	s_mov_b32 s43, s11
	s_lshl_b64 s[64:65], s[6:7], 12
	s_lshl_b64 s[66:67], s[42:43], 12
	v_lshl_add_u64 v[4:5], v[196:197], 0, s[64:65]
	v_lshl_add_u64 v[8:9], v[196:197], 0, s[66:67]
	v_lshl_add_u64 v[246:247], v[198:199], 0, s[64:65]
	s_add_i32 m0, s37, 0xc000
	global_load_dwordx4 v[4:7], v[4:5], off
	s_nop 0
	global_load_dwordx4 v[8:11], v[8:9], off
	s_lshl_b64 s[6:7], s[6:7], 7
	global_load_lds_dwordx4 v[246:247], off
	v_lshl_add_u64 v[246:247], v[198:199], 0, s[66:67]
	s_add_i32 m0, s37, 0xe000
	s_nop 0
	global_load_lds_dwordx4 v[246:247], off
	v_lshl_add_u64 v[246:247], v[16:17], 0, s[6:7]
	s_add_i32 m0, s37, 0x12800
	s_nop 0
	global_load_lds_dwordx4 v[246:247], off
; __device__ __forceinline__ void mask_tile(f32x16& p0, f32x16& p1, int dq, unsigned W) {
;     const float NEG = -__builtin_inff();
; #pragma unroll
;     for (int r = 0; r < 16; ++r) {
;         const int c = (r & 3) + 8 * (r >> 2);
;         if ((unsigned)(dq - c) >= W) p0[r] = NEG;
;         if ((unsigned)(dq - c - 32) >= W) p1[r] = NEG;
;     }
; }
; template <int VB, bool SK>
; __device__ __forceinline__ void pv_tile(f32x16* o, int vb0, bf16x8 pa0, bf16x8 pa1, bf16x8 pa2, bf16x8 pa3, bool act) {
;     if (SK && !act) return;
;     ...
;     if (ATT_PRIO) __builtin_amdgcn_s_setprio(1);
;     PV_D0(0); PV_D0(1); PV_D0(2); PV_D0(3);
.LBB0_1044:
	s_waitcnt lgkmcnt(0)
	s_sub_i32 s6, s42, 33
	v_mfma_f32_32x32x16_bf16 v[66:81], v[12:15], v[230:233], v[66:81]
	ds_read_b64_tr_b16 v[230:231], v209 offset:0x4200
	ds_read_b64_tr_b16 v[232:233], v209 offset:0x4a00
	v_mfma_f32_32x32x16_bf16 v[66:81], v[178:181], v[234:237], v[66:81]
	ds_read_b64_tr_b16 v[234:235], v209 offset:0x5200
	ds_read_b64_tr_b16 v[236:237], v209 offset:0x5a00
	v_mfma_f32_32x32x16_bf16 v[66:81], v[182:185], v[238:241], v[66:81]
	ds_read_b64_tr_b16 v[238:239], v209 offset:0x6200
	ds_read_b64_tr_b16 v[240:241], v209 offset:0x6a00
	ds_read_b64_tr_b16 v[246:247], v209 offset:0x7200
	ds_read_b64_tr_b16 v[248:249], v209 offset:0x7a00
	s_waitcnt lgkmcnt(0)
	v_mfma_f32_32x32x16_bf16 v[66:81], v[186:189], v[242:245], v[66:81]
	v_mfma_f32_32x32x16_bf16 v[50:65], v[12:15], v[230:233], v[50:65]
	ds_read_b64_tr_b16 v[230:231], v209 offset:0x4400
	ds_read_b64_tr_b16 v[232:233], v209 offset:0x4c00
	v_mfma_f32_32x32x16_bf16 v[50:65], v[178:181], v[234:237], v[50:65]
	ds_read_b64_tr_b16 v[234:235], v209 offset:0x5400
	ds_read_b64_tr_b16 v[236:237], v209 offset:0x5c00
	v_mfma_f32_32x32x16_bf16 v[50:65], v[182:185], v[238:241], v[50:65]
	ds_read_b64_tr_b16 v[238:239], v209 offset:0x6400
	ds_read_b64_tr_b16 v[240:241], v209 offset:0x6c00
	ds_read_b64_tr_b16 v[242:243], v209 offset:0x7400
	ds_read_b64_tr_b16 v[244:245], v209 offset:0x7c00
	s_waitcnt lgkmcnt(0)
	v_mfma_f32_32x32x16_bf16 v[50:65], v[186:189], v[246:249], v[50:65]
	v_mfma_f32_32x32x16_bf16 v[34:49], v[12:15], v[230:233], v[34:49]
	ds_read_b64_tr_b16 v[230:231], v209 offset:0x4600
	ds_read_b64_tr_b16 v[232:233], v209 offset:0x4e00
	v_mfma_f32_32x32x16_bf16 v[34:49], v[178:181], v[234:237], v[34:49]
	ds_read_b64_tr_b16 v[234:235], v209 offset:0x5600
	ds_read_b64_tr_b16 v[236:237], v209 offset:0x5e00
	v_mfma_f32_32x32x16_bf16 v[34:49], v[182:185], v[238:241], v[34:49]
	ds_read_b64_tr_b16 v[238:239], v209 offset:0x6600
	ds_read_b64_tr_b16 v[240:241], v209 offset:0x6e00
	ds_read_b64_tr_b16 v[246:247], v209 offset:0x7600
	ds_read_b64_tr_b16 v[248:249], v209 offset:0x7e00
	s_waitcnt lgkmcnt(0)
	v_mfma_f32_32x32x16_bf16 v[34:49], v[186:189], v[242:245], v[34:49]
	v_mfma_f32_32x32x16_bf16 v[18:33], v[12:15], v[230:233], v[18:33]
	s_cmp_le_i32 s6, s40
	s_cselect_b64 s[6:7], -1, 0
	s_cmp_gt_i32 s10, s60
	s_cselect_b64 s[64:65], -1, 0
	s_and_b64 s[6:7], s[64:65], s[6:7]
	s_and_b64 vcc, exec, s[6:7]
	v_mfma_f32_32x32x16_bf16 v[18:33], v[178:181], v[234:237], v[18:33]
	v_mfma_f32_32x32x16_bf16 v[18:33], v[182:185], v[238:241], v[18:33]
	v_mfma_f32_32x32x16_bf16 v[18:33], v[186:189], v[246:249], v[18:33]
	s_cbranch_vccnz .LBB0_1046
	v_add_u32_e32 v12, 59, v193
	v_cmp_gt_u32_e32 vcc, 2.0, v12
	v_add_u32_e32 v12, 27, v193
	s_nop 0
	v_cndmask_b32_e32 v130, v200, v130, vcc
	v_cmp_gt_u32_e32 vcc, 2.0, v12
	v_add_u32_e32 v12, 58, v193
	s_nop 0
	v_cndmask_b32_e32 v114, v200, v114, vcc
	v_cmp_gt_u32_e32 vcc, 2.0, v12
	v_add_u32_e32 v12, 26, v193
	s_nop 0
	v_cndmask_b32_e32 v131, v200, v131, vcc
	v_cmp_gt_u32_e32 vcc, 2.0, v12
	v_add_u32_e32 v12, 57, v193
	s_nop 0
	v_cndmask_b32_e32 v115, v200, v115, vcc
	v_cmp_gt_u32_e32 vcc, 2.0, v12
	v_add_u32_e32 v12, 25, v193
	s_nop 0
	v_cndmask_b32_e32 v132, v200, v132, vcc
	v_cmp_gt_u32_e32 vcc, 2.0, v12
	v_add_u32_e32 v12, 56, v193
	s_nop 0
	v_cndmask_b32_e32 v116, v200, v116, vcc
	v_cmp_gt_u32_e32 vcc, 2.0, v12
	v_add_u32_e32 v12, 24, v193
	s_nop 0
	v_cndmask_b32_e32 v133, v200, v133, vcc
	v_cmp_gt_u32_e32 vcc, 2.0, v12
	v_add_u32_e32 v12, 51, v193
	s_nop 0
	v_cndmask_b32_e32 v117, v200, v117, vcc
	v_cmp_gt_u32_e32 vcc, 2.0, v12
	v_add_u32_e32 v12, 19, v193
	s_nop 0
	v_cndmask_b32_e32 v134, v200, v134, vcc
	v_cmp_gt_u32_e32 vcc, 2.0, v12
	v_add_u32_e32 v12, 50, v193
	s_nop 0
	v_cndmask_b32_e32 v118, v200, v118, vcc
	v_cmp_gt_u32_e32 vcc, 2.0, v12
	v_add_u32_e32 v12, 18, v193
	s_nop 0
	v_cndmask_b32_e32 v135, v200, v135, vcc
	v_cmp_gt_u32_e32 vcc, 2.0, v12
	v_add_u32_e32 v12, 49, v193
	s_nop 0
	v_cndmask_b32_e32 v119, v200, v119, vcc
	v_cmp_gt_u32_e32 vcc, 2.0, v12
	v_add_u32_e32 v12, 17, v193
	s_nop 0
	v_cndmask_b32_e32 v136, v200, v136, vcc
	v_cmp_gt_u32_e32 vcc, 2.0, v12
	v_add_u32_e32 v12, 48, v193
	s_nop 0
	v_cndmask_b32_e32 v120, v200, v120, vcc
	v_cmp_gt_u32_e32 vcc, 2.0, v12
	v_add_u32_e32 v12, 16, v193
	s_nop 0
	v_cndmask_b32_e32 v137, v200, v137, vcc
	v_cmp_gt_u32_e32 vcc, 2.0, v12
	v_add_u32_e32 v12, 43, v193
	s_nop 0
	v_cndmask_b32_e32 v121, v200, v121, vcc
	v_cmp_gt_u32_e32 vcc, 2.0, v12
	v_add_u32_e32 v12, 11, v193
	s_nop 0
	v_cndmask_b32_e32 v138, v200, v138, vcc
	v_cmp_gt_u32_e32 vcc, 2.0, v12
	v_add_u32_e32 v12, 42, v193
	s_nop 0
	v_cndmask_b32_e32 v122, v200, v122, vcc
	v_cmp_gt_u32_e32 vcc, 2.0, v12
	v_add_u32_e32 v12, 10, v193
	s_nop 0
	v_cndmask_b32_e32 v139, v200, v139, vcc
	v_cmp_gt_u32_e32 vcc, 2.0, v12
	v_add_u32_e32 v12, 41, v193
	s_nop 0
	v_cndmask_b32_e32 v123, v200, v123, vcc
	v_cmp_gt_u32_e32 vcc, 2.0, v12
	v_add_u32_e32 v12, 9, v193
	s_nop 0
	v_cndmask_b32_e32 v140, v200, v140, vcc
	v_cmp_gt_u32_e32 vcc, 2.0, v12
	v_add_u32_e32 v12, 40, v193
	s_nop 0
	v_cndmask_b32_e32 v124, v200, v124, vcc
	v_cmp_gt_u32_e32 vcc, 2.0, v12
	v_add_u32_e32 v12, 8, v193
	s_nop 0
	v_cndmask_b32_e32 v141, v200, v141, vcc
	v_cmp_gt_u32_e32 vcc, 2.0, v12
	v_add_u32_e32 v12, 35, v193
	s_nop 0
	v_cndmask_b32_e32 v125, v200, v125, vcc
	v_cmp_gt_u32_e32 vcc, 2.0, v12
	v_add_u32_e32 v12, 3, v193
	s_nop 0
	v_cndmask_b32_e32 v142, v200, v142, vcc
	v_cmp_gt_u32_e32 vcc, 2.0, v12
	v_add_u32_e32 v12, 34, v193
	s_nop 0
	v_cndmask_b32_e32 v126, v200, v126, vcc
	v_cmp_gt_u32_e32 vcc, 2.0, v12
	v_add_u32_e32 v12, 2, v193
	s_nop 0
	v_cndmask_b32_e32 v143, v200, v143, vcc
	v_cmp_gt_u32_e32 vcc, 2.0, v12
	v_add_u32_e32 v12, 33, v193
	s_nop 0
	v_cndmask_b32_e32 v127, v200, v127, vcc
	v_cmp_gt_u32_e32 vcc, 2.0, v12
	v_add_u32_e32 v12, 1, v193
	s_nop 0
	v_cndmask_b32_e32 v144, v200, v144, vcc
	v_cmp_gt_u32_e32 vcc, 2.0, v12
	v_add_u32_e32 v12, 32, v193
	s_nop 0
	v_cndmask_b32_e32 v128, v200, v128, vcc
	v_cmp_gt_u32_e32 vcc, 2.0, v12
	s_nop 1
	v_cndmask_b32_e32 v145, v200, v145, vcc
	v_cmp_gt_u32_e32 vcc, 2.0, v193
	s_nop 1
	v_cndmask_b32_e32 v129, v200, v129, vcc
